# fused fp8 schedule + prio2 + gates epilogue mul fold + single hazard pad + P10 routing scalar bias + global epilogue ld/st
# speedup vs baseline: 1.0067x; 1.0067x over previous
; __device__ __forceinline__ unsigned pk_bf16(float lo, float hi) { const bf16x2_t r = __builtin_convertvector((f32x2){lo, hi}, bf16x2_t); return __builtin_bit_cast(unsigned, r); }
; __device__ __forceinline__ float fsigmoid(float x) { return __builtin_amdgcn_rcpf(1.0f + __builtin_amdgcn_exp2f(-1.44269504f * x)); }
; __device__ __forceinline__ void st16_bf16(bf16* dst, f32x4 a, f32x4 b, f32x4 c, f32x4 d) {
;     u32x4 w0, w1; w0.x = pk_bf16(a[0], a[1]); w0.y = pk_bf16(a[2], a[3]); w0.z = pk_bf16(b[0], b[1]); w0.w = pk_bf16(b[2], b[3]);
;     w1.x = pk_bf16(c[0], c[1]); w1.y = pk_bf16(c[2], c[3]); w1.z = pk_bf16(d[0], d[1]); w1.w = pk_bf16(d[2], d[3]);
;     *(u32x4*)dst = w0; *(u32x4*)(dst + 8) = w1; }
; __device__ __forceinline__ unsigned pk4_u8(float a, float b, float c, float d) {
;     const unsigned ya = __builtin_bit_cast(unsigned, a * 255.0f + 8388608.0f), yb = __builtin_bit_cast(unsigned, b * 255.0f + 8388608.0f), yc = __builtin_bit_cast(unsigned, c * 255.0f + 8388608.0f), yd = __builtin_bit_cast(unsigned, d * 255.0f + 8388608.0f);
;     const unsigned w01 = __builtin_amdgcn_perm(yb, ya, 0x0c0c0400u), w23 = __builtin_amdgcn_perm(yd, yc, 0x0c0c0400u);
;     return __builtin_amdgcn_perm(w23, w01, 0x05040100u); }
;     __device__ __forceinline__ void operator()(AccRef acc, const GUnit& u, int wr, int wc, int fr, int fq) const {
;         const int pm = u.x0, pn = u.x1; unsigned char* base = (pn < 8 ? GZF : GZS) + (size_t)(pm * 256 + wr * 64 + fr) * D + (pn & 7) * 256 + wc * 64 + 16 * fq;
; #pragma unroll
;         for (int ai = 0; ai < 2; ++ai)
; #pragma unroll
;             for (int m = 0; m < 4; ++m) { u32x4 w;
; #pragma unroll
;                 for (int bj = 0; bj < 2; ++bj)
; #pragma unroll
;                     for (int n = 0; n < 2; ++n) { const f32x4 v = acc[ai][bj][m][n]; w[bj * 2 + n] = pk4_u8(fsigmoid(v[0] * W8_INV), fsigmoid(v[1] * W8_INV), fsigmoid(v[2] * W8_INV), fsigmoid(v[3] * W8_INV)); }
;                 *(u32x4*)(base + (size_t)(ai * 128 + m * 16) * D) = w; }
;     }
.LBB0_431:
	s_nop 15
	s_nop 7
	v_lshl_add_u32 v2, s8, 8, v190
	v_mul_f32_e32 v4, 0xbcb8aa3b, v158
	v_mul_f32_e32 v5, 0xbcb8aa3b, v159
	v_mul_f32_e32 v6, 0xbcb8aa3b, v160
	v_mul_f32_e32 v7, 0xbcb8aa3b, v161
	v_exp_f32_e32 v4, v4
	v_exp_f32_e32 v5, v5
	v_exp_f32_e32 v6, v6
	v_exp_f32_e32 v7, v7
	v_add_f32_e32 v4, 1.0, v4
	v_add_f32_e32 v5, 1.0, v5
	v_add_f32_e32 v6, 1.0, v6
	v_add_f32_e32 v7, 1.0, v7
	v_rcp_f32_e32 v4, v4
	v_rcp_f32_e32 v5, v5
	v_rcp_f32_e32 v6, v6
	v_rcp_f32_e32 v7, v7
	v_fmamk_f32 v4, v4, 0x437f0000, v196
	v_fmamk_f32 v5, v5, 0x437f0000, v196
	v_fmamk_f32 v6, v6, 0x437f0000, v196
	v_fmamk_f32 v7, v7, 0x437f0000, v196
	v_perm_b32 v4, v5, v4, s67
	v_perm_b32 v5, v7, v6, s67
	v_mul_f32_e32 v6, 0xbcb8aa3b, v154
	v_mul_f32_e32 v7, 0xbcb8aa3b, v155
	v_exp_f32_e32 v6, v6
	v_exp_f32_e32 v7, v7
	v_perm_b32 v4, v5, v4, s68
	v_add_f32_e32 v5, 1.0, v6
	v_add_f32_e32 v6, 1.0, v7
	v_mul_f32_e32 v7, 0xbcb8aa3b, v156
	v_mul_f32_e32 v8, 0xbcb8aa3b, v157
	v_exp_f32_e32 v7, v7
	v_exp_f32_e32 v8, v8
	v_rcp_f32_e32 v5, v5
	v_rcp_f32_e32 v6, v6
	v_add_f32_e32 v7, 1.0, v7
	v_add_f32_e32 v8, 1.0, v8
	v_rcp_f32_e32 v7, v7
	v_rcp_f32_e32 v8, v8
	v_fmamk_f32 v5, v5, 0x437f0000, v196
	v_fmamk_f32 v6, v6, 0x437f0000, v196
	v_fmamk_f32 v7, v7, 0x437f0000, v196
	v_fmamk_f32 v8, v8, 0x437f0000, v196
	v_perm_b32 v5, v6, v5, s67
	v_perm_b32 v6, v8, v7, s67
	v_mul_f32_e32 v7, 0xbcb8aa3b, v150
	v_mul_f32_e32 v8, 0xbcb8aa3b, v151
	v_exp_f32_e32 v7, v7
	v_exp_f32_e32 v8, v8
	v_perm_b32 v5, v6, v5, s68
	v_add_f32_e32 v6, 1.0, v7
	v_add_f32_e32 v7, 1.0, v8
	v_mul_f32_e32 v8, 0xbcb8aa3b, v152
	v_mul_f32_e32 v9, 0xbcb8aa3b, v153
	v_exp_f32_e32 v8, v8
	v_exp_f32_e32 v9, v9
	v_rcp_f32_e32 v6, v6
	v_rcp_f32_e32 v7, v7
	v_add_f32_e32 v8, 1.0, v8
	v_add_f32_e32 v9, 1.0, v9
	v_rcp_f32_e32 v8, v8
	v_rcp_f32_e32 v9, v9
	v_fmamk_f32 v6, v6, 0x437f0000, v196
	v_fmamk_f32 v7, v7, 0x437f0000, v196
	v_fmamk_f32 v8, v8, 0x437f0000, v196
	v_fmamk_f32 v9, v9, 0x437f0000, v196
	v_perm_b32 v6, v7, v6, s67
	v_perm_b32 v7, v9, v8, s67
	v_mul_f32_e32 v8, 0xbcb8aa3b, v146
	v_mul_f32_e32 v9, 0xbcb8aa3b, v147
	v_exp_f32_e32 v8, v8
	v_exp_f32_e32 v9, v9
	v_perm_b32 v6, v7, v6, s68
	v_add_f32_e32 v7, 1.0, v8
	v_add_f32_e32 v8, 1.0, v9
	v_mul_f32_e32 v9, 0xbcb8aa3b, v148
	v_mul_f32_e32 v10, 0xbcb8aa3b, v149
	v_exp_f32_e32 v9, v9
	v_exp_f32_e32 v10, v10
	v_rcp_f32_e32 v7, v7
	v_rcp_f32_e32 v8, v8
	v_add_f32_e32 v9, 1.0, v9
	v_add_f32_e32 v10, 1.0, v10
	v_rcp_f32_e32 v9, v9
	v_rcp_f32_e32 v10, v10
	s_cmp_lt_i32 s73, 8
	v_ashrrev_i32_e32 v3, 31, v2
	s_cselect_b32 s25, s41, s59
	s_cselect_b32 s24, s40, s53
	v_lshlrev_b64 v[2:3], 11, v[2:3]
	s_lshl_b32 s8, s73, 8
	v_lshl_add_u64 v[2:3], s[24:25], 0, v[2:3]
	s_and_b32 s8, s8, 0x700
	v_lshl_add_u64 v[2:3], v[2:3], 0, s[8:9]
	v_fmamk_f32 v7, v7, 0x437f0000, v196
	v_fmamk_f32 v8, v8, 0x437f0000, v196
	v_fmamk_f32 v9, v9, 0x437f0000, v196
	v_fmamk_f32 v10, v10, 0x437f0000, v196
	v_lshl_add_u64 v[2:3], v[2:3], 0, s[14:15]
	v_perm_b32 v7, v8, v7, s67
	v_perm_b32 v8, v10, v9, s67
	v_lshl_add_u64 v[2:3], v[2:3], 0, v[162:163]
	v_perm_b32 v7, v8, v7, s68
	global_store_dwordx4 v[2:3], v[4:7], off
	v_mul_f32_e32 v8, 0xbcb8aa3b, v142
	v_mul_f32_e32 v9, 0xbcb8aa3b, v143
	v_mul_f32_e32 v6, 0xbcb8aa3b, v144
	v_mul_f32_e32 v7, 0xbcb8aa3b, v145
	v_exp_f32_e32 v8, v8
	v_exp_f32_e32 v9, v9
	v_exp_f32_e32 v6, v6
	v_exp_f32_e32 v7, v7
	v_add_f32_e32 v4, 1.0, v8
	v_add_f32_e32 v5, 1.0, v9
	v_add_f32_e32 v6, 1.0, v6
	v_add_f32_e32 v7, 1.0, v7
	v_rcp_f32_e32 v4, v4
	v_rcp_f32_e32 v5, v5
	v_rcp_f32_e32 v6, v6
	v_rcp_f32_e32 v7, v7
	v_fmamk_f32 v4, v4, 0x437f0000, v196
	v_fmamk_f32 v5, v5, 0x437f0000, v196
	v_fmamk_f32 v6, v6, 0x437f0000, v196
	v_fmamk_f32 v7, v7, 0x437f0000, v196
	v_perm_b32 v4, v5, v4, s67
	v_perm_b32 v5, v7, v6, s67
	v_mul_f32_e32 v6, 0xbcb8aa3b, v138
	v_mul_f32_e32 v7, 0xbcb8aa3b, v139
	v_exp_f32_e32 v6, v6
	v_exp_f32_e32 v7, v7
	v_perm_b32 v4, v5, v4, s68
	v_add_f32_e32 v5, 1.0, v6
	v_add_f32_e32 v6, 1.0, v7
	v_mul_f32_e32 v7, 0xbcb8aa3b, v140
	v_mul_f32_e32 v8, 0xbcb8aa3b, v141
	v_exp_f32_e32 v7, v7
	v_exp_f32_e32 v8, v8
	v_rcp_f32_e32 v5, v5
	v_rcp_f32_e32 v6, v6
	v_add_f32_e32 v7, 1.0, v7
	v_add_f32_e32 v8, 1.0, v8
	v_rcp_f32_e32 v7, v7
	v_rcp_f32_e32 v8, v8
	v_fmamk_f32 v5, v5, 0x437f0000, v196
	v_fmamk_f32 v6, v6, 0x437f0000, v196
	v_fmamk_f32 v7, v7, 0x437f0000, v196
	v_fmamk_f32 v8, v8, 0x437f0000, v196
	v_perm_b32 v5, v6, v5, s67
	v_perm_b32 v6, v8, v7, s67
	v_mul_f32_e32 v7, 0xbcb8aa3b, v134
	v_mul_f32_e32 v8, 0xbcb8aa3b, v135
	v_exp_f32_e32 v7, v7
	v_exp_f32_e32 v8, v8
	v_perm_b32 v5, v6, v5, s68
	v_add_f32_e32 v6, 1.0, v7
	v_add_f32_e32 v7, 1.0, v8
	v_mul_f32_e32 v8, 0xbcb8aa3b, v136
	v_mul_f32_e32 v9, 0xbcb8aa3b, v137
	v_exp_f32_e32 v8, v8
	v_exp_f32_e32 v9, v9
	v_rcp_f32_e32 v6, v6
	v_rcp_f32_e32 v7, v7
	v_add_f32_e32 v8, 1.0, v8
	v_add_f32_e32 v9, 1.0, v9
	v_rcp_f32_e32 v8, v8
	v_rcp_f32_e32 v9, v9
	v_fmamk_f32 v6, v6, 0x437f0000, v196
	v_fmamk_f32 v7, v7, 0x437f0000, v196
	v_fmamk_f32 v8, v8, 0x437f0000, v196
	v_fmamk_f32 v9, v9, 0x437f0000, v196
	v_perm_b32 v6, v7, v6, s67
	v_perm_b32 v7, v9, v8, s67
	v_mul_f32_e32 v8, 0xbcb8aa3b, v130
	v_mul_f32_e32 v9, 0xbcb8aa3b, v131
	v_exp_f32_e32 v8, v8
	v_exp_f32_e32 v9, v9
	v_perm_b32 v6, v7, v6, s68
	v_add_f32_e32 v7, 1.0, v8
	v_add_f32_e32 v8, 1.0, v9
	v_mul_f32_e32 v9, 0xbcb8aa3b, v132
	v_mul_f32_e32 v10, 0xbcb8aa3b, v133
	v_exp_f32_e32 v9, v9
	v_exp_f32_e32 v10, v10
	v_rcp_f32_e32 v7, v7
	v_rcp_f32_e32 v8, v8
	v_add_f32_e32 v9, 1.0, v9
	v_add_f32_e32 v10, 1.0, v10
	v_rcp_f32_e32 v9, v9
	v_rcp_f32_e32 v10, v10
	v_fmamk_f32 v7, v7, 0x437f0000, v196
	v_fmamk_f32 v8, v8, 0x437f0000, v196
; __device__ __forceinline__ unsigned pk_bf16(float lo, float hi) { const bf16x2_t r = __builtin_convertvector((f32x2){lo, hi}, bf16x2_t); return __builtin_bit_cast(unsigned, r); }
; __device__ __forceinline__ float fsigmoid(float x) { return __builtin_amdgcn_rcpf(1.0f + __builtin_amdgcn_exp2f(-1.44269504f * x)); }
; __device__ __forceinline__ void st16_bf16(bf16* dst, f32x4 a, f32x4 b, f32x4 c, f32x4 d) {
;     u32x4 w0, w1; w0.x = pk_bf16(a[0], a[1]); w0.y = pk_bf16(a[2], a[3]); w0.z = pk_bf16(b[0], b[1]); w0.w = pk_bf16(b[2], b[3]);
;     w1.x = pk_bf16(c[0], c[1]); w1.y = pk_bf16(c[2], c[3]); w1.z = pk_bf16(d[0], d[1]); w1.w = pk_bf16(d[2], d[3]);
;     *(u32x4*)dst = w0; *(u32x4*)(dst + 8) = w1; }
; __device__ __forceinline__ unsigned pk4_u8(float a, float b, float c, float d) {
;     const unsigned ya = __builtin_bit_cast(unsigned, a * 255.0f + 8388608.0f), yb = __builtin_bit_cast(unsigned, b * 255.0f + 8388608.0f), yc = __builtin_bit_cast(unsigned, c * 255.0f + 8388608.0f), yd = __builtin_bit_cast(unsigned, d * 255.0f + 8388608.0f);
;     const unsigned w01 = __builtin_amdgcn_perm(yb, ya, 0x0c0c0400u), w23 = __builtin_amdgcn_perm(yd, yc, 0x0c0c0400u);
;     return __builtin_amdgcn_perm(w23, w01, 0x05040100u); }
;     __device__ __forceinline__ void operator()(AccRef acc, const GUnit& u, int wr, int wc, int fr, int fq) const {
;         const int pm = u.x0, pn = u.x1; unsigned char* base = (pn < 8 ? GZF : GZS) + (size_t)(pm * 256 + wr * 64 + fr) * D + (pn & 7) * 256 + wc * 64 + 16 * fq;
; #pragma unroll
;         for (int ai = 0; ai < 2; ++ai)
; #pragma unroll
;             for (int m = 0; m < 4; ++m) { u32x4 w;
; #pragma unroll
;                 for (int bj = 0; bj < 2; ++bj)
; #pragma unroll
;                     for (int n = 0; n < 2; ++n) { const f32x4 v = acc[ai][bj][m][n]; w[bj * 2 + n] = pk4_u8(fsigmoid(v[0] * W8_INV), fsigmoid(v[1] * W8_INV), fsigmoid(v[2] * W8_INV), fsigmoid(v[3] * W8_INV)); }
;                 *(u32x4*)(base + (size_t)(ai * 128 + m * 16) * D) = w; }
;     }
	v_fmamk_f32 v9, v9, 0x437f0000, v196
	v_fmamk_f32 v10, v10, 0x437f0000, v196
	v_perm_b32 v7, v8, v7, s67
	v_perm_b32 v8, v10, v9, s67
	v_perm_b32 v7, v8, v7, s68
	v_add_co_u32_e32 v8, vcc, s63, v2
	s_nop 0
	s_nop 0
	v_addc_co_u32_e32 v9, vcc, 0, v3, vcc
	global_store_dwordx4 v[8:9], v[4:7], off
	v_mul_f32_e32 v10, 0xbcb8aa3b, v126
	v_mul_f32_e32 v11, 0xbcb8aa3b, v127
	v_mul_f32_e32 v6, 0xbcb8aa3b, v128
	v_mul_f32_e32 v7, 0xbcb8aa3b, v129
	v_exp_f32_e32 v10, v10
	v_exp_f32_e32 v11, v11
	v_exp_f32_e32 v6, v6
	v_exp_f32_e32 v7, v7
	v_add_f32_e32 v4, 1.0, v10
	v_add_f32_e32 v5, 1.0, v11
	v_add_f32_e32 v6, 1.0, v6
	v_add_f32_e32 v7, 1.0, v7
	v_rcp_f32_e32 v4, v4
	v_rcp_f32_e32 v5, v5
	v_rcp_f32_e32 v6, v6
	v_rcp_f32_e32 v7, v7
	v_fmamk_f32 v4, v4, 0x437f0000, v196
	v_fmamk_f32 v5, v5, 0x437f0000, v196
	v_fmamk_f32 v6, v6, 0x437f0000, v196
	v_fmamk_f32 v7, v7, 0x437f0000, v196
	v_perm_b32 v4, v5, v4, s67
	v_perm_b32 v5, v7, v6, s67
	v_mul_f32_e32 v6, 0xbcb8aa3b, v122
	v_mul_f32_e32 v7, 0xbcb8aa3b, v123
	v_exp_f32_e32 v6, v6
	v_exp_f32_e32 v7, v7
	v_perm_b32 v4, v5, v4, s68
	v_add_f32_e32 v5, 1.0, v6
	v_add_f32_e32 v6, 1.0, v7
	v_mul_f32_e32 v7, 0xbcb8aa3b, v124
	v_mul_f32_e32 v8, 0xbcb8aa3b, v125
	v_exp_f32_e32 v7, v7
	v_exp_f32_e32 v8, v8
	v_rcp_f32_e32 v5, v5
	v_rcp_f32_e32 v6, v6
	v_add_f32_e32 v7, 1.0, v7
	v_add_f32_e32 v8, 1.0, v8
	v_rcp_f32_e32 v7, v7
	v_rcp_f32_e32 v8, v8
	v_fmamk_f32 v5, v5, 0x437f0000, v196
	v_fmamk_f32 v6, v6, 0x437f0000, v196
	v_fmamk_f32 v7, v7, 0x437f0000, v196
	v_fmamk_f32 v8, v8, 0x437f0000, v196
	v_perm_b32 v5, v6, v5, s67
	v_perm_b32 v6, v8, v7, s67
	v_mul_f32_e32 v7, 0xbcb8aa3b, v118
	v_mul_f32_e32 v8, 0xbcb8aa3b, v119
	v_exp_f32_e32 v7, v7
	v_exp_f32_e32 v8, v8
	v_perm_b32 v5, v6, v5, s68
	v_add_f32_e32 v6, 1.0, v7
	v_add_f32_e32 v7, 1.0, v8
	v_mul_f32_e32 v8, 0xbcb8aa3b, v120
	v_mul_f32_e32 v9, 0xbcb8aa3b, v121
	v_exp_f32_e32 v8, v8
	v_exp_f32_e32 v9, v9
	v_rcp_f32_e32 v6, v6
	v_rcp_f32_e32 v7, v7
	v_add_f32_e32 v8, 1.0, v8
	v_add_f32_e32 v9, 1.0, v9
	v_rcp_f32_e32 v8, v8
	v_rcp_f32_e32 v9, v9
	v_fmamk_f32 v6, v6, 0x437f0000, v196
	v_fmamk_f32 v7, v7, 0x437f0000, v196
	v_fmamk_f32 v8, v8, 0x437f0000, v196
	v_fmamk_f32 v9, v9, 0x437f0000, v196
	v_perm_b32 v6, v7, v6, s67
	v_perm_b32 v7, v9, v8, s67
	v_mul_f32_e32 v8, 0xbcb8aa3b, v114
	v_mul_f32_e32 v9, 0xbcb8aa3b, v115
	v_exp_f32_e32 v8, v8
	v_exp_f32_e32 v9, v9
	v_perm_b32 v6, v7, v6, s68
	v_add_f32_e32 v7, 1.0, v8
	v_add_f32_e32 v8, 1.0, v9
	v_mul_f32_e32 v9, 0xbcb8aa3b, v116
	v_mul_f32_e32 v10, 0xbcb8aa3b, v117
	v_exp_f32_e32 v9, v9
	v_exp_f32_e32 v10, v10
	v_rcp_f32_e32 v7, v7
	v_rcp_f32_e32 v8, v8
	v_add_f32_e32 v9, 1.0, v9
	v_add_f32_e32 v10, 1.0, v10
	v_rcp_f32_e32 v9, v9
	v_rcp_f32_e32 v10, v10
	v_fmamk_f32 v7, v7, 0x437f0000, v196
	v_fmamk_f32 v8, v8, 0x437f0000, v196
	v_fmamk_f32 v9, v9, 0x437f0000, v196
	v_fmamk_f32 v10, v10, 0x437f0000, v196
	v_perm_b32 v7, v8, v7, s67
	v_perm_b32 v8, v10, v9, s67
	v_perm_b32 v7, v8, v7, s68
	v_add_co_u32_e32 v8, vcc, s52, v2
	s_nop 0
	s_nop 0
	v_addc_co_u32_e32 v9, vcc, 0, v3, vcc
	global_store_dwordx4 v[8:9], v[4:7], off
	v_mul_f32_e32 v10, 0xbcb8aa3b, v110
	v_mul_f32_e32 v11, 0xbcb8aa3b, v111
	v_mul_f32_e32 v6, 0xbcb8aa3b, v112
	v_mul_f32_e32 v7, 0xbcb8aa3b, v113
	v_exp_f32_e32 v10, v10
	v_exp_f32_e32 v11, v11
	v_exp_f32_e32 v6, v6
	v_exp_f32_e32 v7, v7
	v_add_f32_e32 v4, 1.0, v10
	v_add_f32_e32 v5, 1.0, v11
	v_add_f32_e32 v6, 1.0, v6
	v_add_f32_e32 v7, 1.0, v7
	v_rcp_f32_e32 v4, v4
	v_rcp_f32_e32 v5, v5
	v_rcp_f32_e32 v6, v6
	v_rcp_f32_e32 v7, v7
	v_fmamk_f32 v4, v4, 0x437f0000, v196
	v_fmamk_f32 v5, v5, 0x437f0000, v196
	v_fmamk_f32 v6, v6, 0x437f0000, v196
	v_fmamk_f32 v7, v7, 0x437f0000, v196
	v_perm_b32 v4, v5, v4, s67
	v_perm_b32 v5, v7, v6, s67
	v_mul_f32_e32 v6, 0xbcb8aa3b, v106
	v_mul_f32_e32 v7, 0xbcb8aa3b, v107
	v_exp_f32_e32 v6, v6
	v_exp_f32_e32 v7, v7
	v_perm_b32 v4, v5, v4, s68
	v_add_f32_e32 v5, 1.0, v6
	v_add_f32_e32 v6, 1.0, v7
	v_mul_f32_e32 v7, 0xbcb8aa3b, v108
	v_mul_f32_e32 v8, 0xbcb8aa3b, v109
	v_exp_f32_e32 v7, v7
	v_exp_f32_e32 v8, v8
	v_rcp_f32_e32 v5, v5
	v_rcp_f32_e32 v6, v6
	v_add_f32_e32 v7, 1.0, v7
	v_add_f32_e32 v8, 1.0, v8
	v_rcp_f32_e32 v7, v7
	v_rcp_f32_e32 v8, v8
	v_fmamk_f32 v5, v5, 0x437f0000, v196
	v_fmamk_f32 v6, v6, 0x437f0000, v196
	v_fmamk_f32 v7, v7, 0x437f0000, v196
	v_fmamk_f32 v8, v8, 0x437f0000, v196
	v_perm_b32 v5, v6, v5, s67
	v_perm_b32 v6, v8, v7, s67
	v_mul_f32_e32 v7, 0xbcb8aa3b, v102
	v_mul_f32_e32 v8, 0xbcb8aa3b, v103
	v_exp_f32_e32 v7, v7
	v_exp_f32_e32 v8, v8
	v_perm_b32 v5, v6, v5, s68
	v_add_f32_e32 v6, 1.0, v7
	v_add_f32_e32 v7, 1.0, v8
	v_mul_f32_e32 v8, 0xbcb8aa3b, v104
	v_mul_f32_e32 v9, 0xbcb8aa3b, v105
	v_exp_f32_e32 v8, v8
	v_exp_f32_e32 v9, v9
	v_rcp_f32_e32 v6, v6
	v_rcp_f32_e32 v7, v7
	v_add_f32_e32 v8, 1.0, v8
	v_add_f32_e32 v9, 1.0, v9
	v_rcp_f32_e32 v8, v8
	v_rcp_f32_e32 v9, v9
	v_fmamk_f32 v6, v6, 0x437f0000, v196
	v_fmamk_f32 v7, v7, 0x437f0000, v196
	v_fmamk_f32 v8, v8, 0x437f0000, v196
	v_fmamk_f32 v9, v9, 0x437f0000, v196
	v_perm_b32 v6, v7, v6, s67
	v_perm_b32 v7, v9, v8, s67
	v_mul_f32_e32 v8, 0xbcb8aa3b, v98
	v_mul_f32_e32 v9, 0xbcb8aa3b, v99
	v_exp_f32_e32 v8, v8
	v_exp_f32_e32 v9, v9
	v_perm_b32 v6, v7, v6, s68
	v_add_f32_e32 v7, 1.0, v8
	v_add_f32_e32 v8, 1.0, v9
	v_mul_f32_e32 v9, 0xbcb8aa3b, v100
	v_mul_f32_e32 v10, 0xbcb8aa3b, v101
	v_exp_f32_e32 v9, v9
	v_exp_f32_e32 v10, v10
	v_rcp_f32_e32 v7, v7
	v_rcp_f32_e32 v8, v8
	v_add_f32_e32 v9, 1.0, v9
	v_add_f32_e32 v10, 1.0, v10
	v_rcp_f32_e32 v9, v9
	v_rcp_f32_e32 v10, v10
	v_fmamk_f32 v7, v7, 0x437f0000, v196
	v_fmamk_f32 v8, v8, 0x437f0000, v196
	v_fmamk_f32 v9, v9, 0x437f0000, v196
; __device__ __forceinline__ unsigned pk_bf16(float lo, float hi) { const bf16x2_t r = __builtin_convertvector((f32x2){lo, hi}, bf16x2_t); return __builtin_bit_cast(unsigned, r); }
; __device__ __forceinline__ float fsigmoid(float x) { return __builtin_amdgcn_rcpf(1.0f + __builtin_amdgcn_exp2f(-1.44269504f * x)); }
; __device__ __forceinline__ void st16_bf16(bf16* dst, f32x4 a, f32x4 b, f32x4 c, f32x4 d) {
;     u32x4 w0, w1; w0.x = pk_bf16(a[0], a[1]); w0.y = pk_bf16(a[2], a[3]); w0.z = pk_bf16(b[0], b[1]); w0.w = pk_bf16(b[2], b[3]);
;     w1.x = pk_bf16(c[0], c[1]); w1.y = pk_bf16(c[2], c[3]); w1.z = pk_bf16(d[0], d[1]); w1.w = pk_bf16(d[2], d[3]);
;     *(u32x4*)dst = w0; *(u32x4*)(dst + 8) = w1; }
; __device__ __forceinline__ unsigned pk4_u8(float a, float b, float c, float d) {
;     const unsigned ya = __builtin_bit_cast(unsigned, a * 255.0f + 8388608.0f), yb = __builtin_bit_cast(unsigned, b * 255.0f + 8388608.0f), yc = __builtin_bit_cast(unsigned, c * 255.0f + 8388608.0f), yd = __builtin_bit_cast(unsigned, d * 255.0f + 8388608.0f);
;     const unsigned w01 = __builtin_amdgcn_perm(yb, ya, 0x0c0c0400u), w23 = __builtin_amdgcn_perm(yd, yc, 0x0c0c0400u);
;     return __builtin_amdgcn_perm(w23, w01, 0x05040100u); }
;     __device__ __forceinline__ void operator()(AccRef acc, const GUnit& u, int wr, int wc, int fr, int fq) const {
;         const int pm = u.x0, pn = u.x1; unsigned char* base = (pn < 8 ? GZF : GZS) + (size_t)(pm * 256 + wr * 64 + fr) * D + (pn & 7) * 256 + wc * 64 + 16 * fq;
; #pragma unroll
;         for (int ai = 0; ai < 2; ++ai)
; #pragma unroll
;             for (int m = 0; m < 4; ++m) { u32x4 w;
; #pragma unroll
;                 for (int bj = 0; bj < 2; ++bj)
; #pragma unroll
;                     for (int n = 0; n < 2; ++n) { const f32x4 v = acc[ai][bj][m][n]; w[bj * 2 + n] = pk4_u8(fsigmoid(v[0] * W8_INV), fsigmoid(v[1] * W8_INV), fsigmoid(v[2] * W8_INV), fsigmoid(v[3] * W8_INV)); }
;                 *(u32x4*)(base + (size_t)(ai * 128 + m * 16) * D) = w; }
;     }
	v_fmamk_f32 v10, v10, 0x437f0000, v196
	v_perm_b32 v7, v8, v7, s67
	v_perm_b32 v8, v10, v9, s67
	v_perm_b32 v7, v8, v7, s68
	v_add_co_u32_e32 v8, vcc, s62, v2
	s_nop 0
	s_nop 0
	v_addc_co_u32_e32 v9, vcc, 0, v3, vcc
	global_store_dwordx4 v[8:9], v[4:7], off
	v_mul_f32_e32 v10, 0xbcb8aa3b, v94
	v_mul_f32_e32 v11, 0xbcb8aa3b, v95
	v_mul_f32_e32 v6, 0xbcb8aa3b, v96
	v_mul_f32_e32 v7, 0xbcb8aa3b, v97
	v_exp_f32_e32 v10, v10
	v_exp_f32_e32 v11, v11
	v_exp_f32_e32 v6, v6
	v_exp_f32_e32 v7, v7
	v_add_f32_e32 v4, 1.0, v10
	v_add_f32_e32 v5, 1.0, v11
	v_add_f32_e32 v6, 1.0, v6
	v_add_f32_e32 v7, 1.0, v7
	v_rcp_f32_e32 v4, v4
	v_rcp_f32_e32 v5, v5
	v_rcp_f32_e32 v6, v6
	v_rcp_f32_e32 v7, v7
	v_fmamk_f32 v4, v4, 0x437f0000, v196
	v_fmamk_f32 v5, v5, 0x437f0000, v196
	v_fmamk_f32 v6, v6, 0x437f0000, v196
	v_fmamk_f32 v7, v7, 0x437f0000, v196
	v_perm_b32 v4, v5, v4, s67
	v_perm_b32 v5, v7, v6, s67
	v_mul_f32_e32 v6, 0xbcb8aa3b, v90
	v_mul_f32_e32 v7, 0xbcb8aa3b, v91
	v_exp_f32_e32 v6, v6
	v_exp_f32_e32 v7, v7
	v_perm_b32 v4, v5, v4, s68
	v_add_f32_e32 v5, 1.0, v6
	v_add_f32_e32 v6, 1.0, v7
	v_mul_f32_e32 v7, 0xbcb8aa3b, v92
	v_mul_f32_e32 v8, 0xbcb8aa3b, v93
	v_exp_f32_e32 v7, v7
	v_exp_f32_e32 v8, v8
	v_rcp_f32_e32 v5, v5
	v_rcp_f32_e32 v6, v6
	v_add_f32_e32 v7, 1.0, v7
	v_add_f32_e32 v8, 1.0, v8
	v_rcp_f32_e32 v7, v7
	v_rcp_f32_e32 v8, v8
	v_fmamk_f32 v5, v5, 0x437f0000, v196
	v_fmamk_f32 v6, v6, 0x437f0000, v196
	v_fmamk_f32 v7, v7, 0x437f0000, v196
	v_fmamk_f32 v8, v8, 0x437f0000, v196
	v_perm_b32 v5, v6, v5, s67
	v_perm_b32 v6, v8, v7, s67
	v_mul_f32_e32 v7, 0xbcb8aa3b, v86
	v_mul_f32_e32 v8, 0xbcb8aa3b, v87
	v_exp_f32_e32 v7, v7
	v_exp_f32_e32 v8, v8
	v_perm_b32 v5, v6, v5, s68
	v_add_f32_e32 v6, 1.0, v7
	v_add_f32_e32 v7, 1.0, v8
	v_mul_f32_e32 v8, 0xbcb8aa3b, v88
	v_mul_f32_e32 v9, 0xbcb8aa3b, v89
	v_exp_f32_e32 v8, v8
	v_exp_f32_e32 v9, v9
	v_rcp_f32_e32 v6, v6
	v_rcp_f32_e32 v7, v7
	v_add_f32_e32 v8, 1.0, v8
	v_add_f32_e32 v9, 1.0, v9
	v_rcp_f32_e32 v8, v8
	v_rcp_f32_e32 v9, v9
	v_fmamk_f32 v6, v6, 0x437f0000, v196
	v_fmamk_f32 v7, v7, 0x437f0000, v196
	v_fmamk_f32 v8, v8, 0x437f0000, v196
	v_fmamk_f32 v9, v9, 0x437f0000, v196
	v_perm_b32 v6, v7, v6, s67
	v_perm_b32 v7, v9, v8, s67
	v_mul_f32_e32 v8, 0xbcb8aa3b, v82
	v_mul_f32_e32 v9, 0xbcb8aa3b, v83
	v_exp_f32_e32 v8, v8
	v_exp_f32_e32 v9, v9
	v_perm_b32 v6, v7, v6, s68
	v_add_f32_e32 v7, 1.0, v8
	v_add_f32_e32 v8, 1.0, v9
	v_mul_f32_e32 v9, 0xbcb8aa3b, v84
	v_mul_f32_e32 v10, 0xbcb8aa3b, v85
	v_exp_f32_e32 v9, v9
	v_exp_f32_e32 v10, v10
	v_rcp_f32_e32 v7, v7
	v_rcp_f32_e32 v8, v8
	v_add_f32_e32 v9, 1.0, v9
	v_add_f32_e32 v10, 1.0, v10
	v_rcp_f32_e32 v9, v9
	v_rcp_f32_e32 v10, v10
	v_fmamk_f32 v7, v7, 0x437f0000, v196
	v_fmamk_f32 v8, v8, 0x437f0000, v196
	v_fmamk_f32 v9, v9, 0x437f0000, v196
	v_fmamk_f32 v10, v10, 0x437f0000, v196
	v_perm_b32 v7, v8, v7, s67
	v_perm_b32 v8, v10, v9, s67
	v_perm_b32 v7, v8, v7, s68
	v_add_co_u32_e32 v8, vcc, s69, v2
	s_nop 0
	s_nop 0
	v_addc_co_u32_e32 v9, vcc, 0, v3, vcc
	global_store_dwordx4 v[8:9], v[4:7], off
	v_mul_f32_e32 v10, 0xbcb8aa3b, v78
	v_mul_f32_e32 v11, 0xbcb8aa3b, v79
	v_mul_f32_e32 v6, 0xbcb8aa3b, v80
	v_mul_f32_e32 v7, 0xbcb8aa3b, v81
	v_exp_f32_e32 v10, v10
	v_exp_f32_e32 v11, v11
	v_exp_f32_e32 v6, v6
	v_exp_f32_e32 v7, v7
	v_add_f32_e32 v4, 1.0, v10
	v_add_f32_e32 v5, 1.0, v11
	v_add_f32_e32 v6, 1.0, v6
	v_add_f32_e32 v7, 1.0, v7
	v_rcp_f32_e32 v4, v4
	v_rcp_f32_e32 v5, v5
	v_rcp_f32_e32 v6, v6
	v_rcp_f32_e32 v7, v7
	v_fmamk_f32 v4, v4, 0x437f0000, v196
	v_fmamk_f32 v5, v5, 0x437f0000, v196
	v_fmamk_f32 v6, v6, 0x437f0000, v196
	v_fmamk_f32 v7, v7, 0x437f0000, v196
	v_perm_b32 v4, v5, v4, s67
	v_perm_b32 v5, v7, v6, s67
	v_mul_f32_e32 v6, 0xbcb8aa3b, v74
	v_mul_f32_e32 v7, 0xbcb8aa3b, v75
	v_exp_f32_e32 v6, v6
	v_exp_f32_e32 v7, v7
	v_perm_b32 v4, v5, v4, s68
	v_add_f32_e32 v5, 1.0, v6
	v_add_f32_e32 v6, 1.0, v7
	v_mul_f32_e32 v7, 0xbcb8aa3b, v76
	v_mul_f32_e32 v8, 0xbcb8aa3b, v77
	v_exp_f32_e32 v7, v7
	v_exp_f32_e32 v8, v8
	v_rcp_f32_e32 v5, v5
	v_rcp_f32_e32 v6, v6
	v_add_f32_e32 v7, 1.0, v7
	v_add_f32_e32 v8, 1.0, v8
	v_rcp_f32_e32 v7, v7
	v_rcp_f32_e32 v8, v8
	v_fmamk_f32 v5, v5, 0x437f0000, v196
	v_fmamk_f32 v6, v6, 0x437f0000, v196
	v_fmamk_f32 v7, v7, 0x437f0000, v196
	v_fmamk_f32 v8, v8, 0x437f0000, v196
	v_perm_b32 v5, v6, v5, s67
	v_perm_b32 v6, v8, v7, s67
	v_mul_f32_e32 v7, 0xbcb8aa3b, v70
	v_mul_f32_e32 v8, 0xbcb8aa3b, v71
	v_exp_f32_e32 v7, v7
	v_exp_f32_e32 v8, v8
	v_perm_b32 v5, v6, v5, s68
	v_add_f32_e32 v6, 1.0, v7
	v_add_f32_e32 v7, 1.0, v8
	v_mul_f32_e32 v8, 0xbcb8aa3b, v72
	v_mul_f32_e32 v9, 0xbcb8aa3b, v73
	v_exp_f32_e32 v8, v8
	v_exp_f32_e32 v9, v9
	v_rcp_f32_e32 v6, v6
	v_rcp_f32_e32 v7, v7
	v_add_f32_e32 v8, 1.0, v8
	v_add_f32_e32 v9, 1.0, v9
	v_rcp_f32_e32 v8, v8
	v_rcp_f32_e32 v9, v9
	v_fmamk_f32 v6, v6, 0x437f0000, v196
	v_fmamk_f32 v7, v7, 0x437f0000, v196
	v_fmamk_f32 v8, v8, 0x437f0000, v196
	v_fmamk_f32 v9, v9, 0x437f0000, v196
	v_perm_b32 v6, v7, v6, s67
	v_perm_b32 v7, v9, v8, s67
	v_mul_f32_e32 v8, 0xbcb8aa3b, v66
	v_mul_f32_e32 v9, 0xbcb8aa3b, v67
	v_exp_f32_e32 v8, v8
	v_exp_f32_e32 v9, v9
	v_perm_b32 v6, v7, v6, s68
	v_add_f32_e32 v7, 1.0, v8
	v_add_f32_e32 v8, 1.0, v9
	v_mul_f32_e32 v9, 0xbcb8aa3b, v68
	v_mul_f32_e32 v10, 0xbcb8aa3b, v69
	v_exp_f32_e32 v9, v9
	v_exp_f32_e32 v10, v10
	v_rcp_f32_e32 v7, v7
	v_rcp_f32_e32 v8, v8
	v_add_f32_e32 v9, 1.0, v9
	v_add_f32_e32 v10, 1.0, v10
	v_rcp_f32_e32 v9, v9
	v_rcp_f32_e32 v10, v10
	v_fmamk_f32 v7, v7, 0x437f0000, v196
	v_fmamk_f32 v8, v8, 0x437f0000, v196
	v_fmamk_f32 v9, v9, 0x437f0000, v196
	v_fmamk_f32 v10, v10, 0x437f0000, v196
	v_perm_b32 v7, v8, v7, s67
; __device__ __forceinline__ unsigned pk_bf16(float lo, float hi) { const bf16x2_t r = __builtin_convertvector((f32x2){lo, hi}, bf16x2_t); return __builtin_bit_cast(unsigned, r); }
; __device__ __forceinline__ float fsigmoid(float x) { return __builtin_amdgcn_rcpf(1.0f + __builtin_amdgcn_exp2f(-1.44269504f * x)); }
; __device__ __forceinline__ void st16_bf16(bf16* dst, f32x4 a, f32x4 b, f32x4 c, f32x4 d) {
;     u32x4 w0, w1; w0.x = pk_bf16(a[0], a[1]); w0.y = pk_bf16(a[2], a[3]); w0.z = pk_bf16(b[0], b[1]); w0.w = pk_bf16(b[2], b[3]);
;     w1.x = pk_bf16(c[0], c[1]); w1.y = pk_bf16(c[2], c[3]); w1.z = pk_bf16(d[0], d[1]); w1.w = pk_bf16(d[2], d[3]);
;     *(u32x4*)dst = w0; *(u32x4*)(dst + 8) = w1; }
; __device__ __forceinline__ unsigned pk4_u8(float a, float b, float c, float d) {
;     const unsigned ya = __builtin_bit_cast(unsigned, a * 255.0f + 8388608.0f), yb = __builtin_bit_cast(unsigned, b * 255.0f + 8388608.0f), yc = __builtin_bit_cast(unsigned, c * 255.0f + 8388608.0f), yd = __builtin_bit_cast(unsigned, d * 255.0f + 8388608.0f);
;     const unsigned w01 = __builtin_amdgcn_perm(yb, ya, 0x0c0c0400u), w23 = __builtin_amdgcn_perm(yd, yc, 0x0c0c0400u);
;     return __builtin_amdgcn_perm(w23, w01, 0x05040100u); }
;     __device__ __forceinline__ void operator()(AccRef acc, const GUnit& u, int wr, int wc, int fr, int fq) const {
;         const int pm = u.x0, pn = u.x1; unsigned char* base = (pn < 8 ? GZF : GZS) + (size_t)(pm * 256 + wr * 64 + fr) * D + (pn & 7) * 256 + wc * 64 + 16 * fq;
; #pragma unroll
;         for (int ai = 0; ai < 2; ++ai)
; #pragma unroll
;             for (int m = 0; m < 4; ++m) { u32x4 w;
; #pragma unroll
;                 for (int bj = 0; bj < 2; ++bj)
; #pragma unroll
;                     for (int n = 0; n < 2; ++n) { const f32x4 v = acc[ai][bj][m][n]; w[bj * 2 + n] = pk4_u8(fsigmoid(v[0] * W8_INV), fsigmoid(v[1] * W8_INV), fsigmoid(v[2] * W8_INV), fsigmoid(v[3] * W8_INV)); }
;                 *(u32x4*)(base + (size_t)(ai * 128 + m * 16) * D) = w; }
;     }
	v_perm_b32 v8, v10, v9, s67
	v_perm_b32 v7, v8, v7, s68
	v_add_co_u32_e32 v8, vcc, s70, v2
	s_nop 0
	s_nop 0
	v_addc_co_u32_e32 v9, vcc, 0, v3, vcc
	global_store_dwordx4 v[8:9], v[4:7], off
	v_mul_f32_e32 v10, 0xbcb8aa3b, v62
	v_mul_f32_e32 v11, 0xbcb8aa3b, v63
	v_mul_f32_e32 v6, 0xbcb8aa3b, v64
	v_mul_f32_e32 v7, 0xbcb8aa3b, v65
	v_exp_f32_e32 v10, v10
	v_exp_f32_e32 v11, v11
	v_exp_f32_e32 v6, v6
	v_exp_f32_e32 v7, v7
	v_add_f32_e32 v4, 1.0, v10
	v_add_f32_e32 v5, 1.0, v11
	v_add_f32_e32 v6, 1.0, v6
	v_add_f32_e32 v7, 1.0, v7
	v_rcp_f32_e32 v4, v4
	v_rcp_f32_e32 v5, v5
	v_rcp_f32_e32 v6, v6
	v_rcp_f32_e32 v7, v7
	v_fmamk_f32 v4, v4, 0x437f0000, v196
	v_fmamk_f32 v5, v5, 0x437f0000, v196
	v_fmamk_f32 v6, v6, 0x437f0000, v196
	v_fmamk_f32 v7, v7, 0x437f0000, v196
	v_perm_b32 v4, v5, v4, s67
	v_perm_b32 v5, v7, v6, s67
	v_mul_f32_e32 v6, 0xbcb8aa3b, v58
	v_mul_f32_e32 v7, 0xbcb8aa3b, v59
	v_exp_f32_e32 v6, v6
	v_exp_f32_e32 v7, v7
	v_perm_b32 v4, v5, v4, s68
	v_add_f32_e32 v5, 1.0, v6
	v_add_f32_e32 v6, 1.0, v7
	v_mul_f32_e32 v7, 0xbcb8aa3b, v60
	v_mul_f32_e32 v8, 0xbcb8aa3b, v61
	v_exp_f32_e32 v7, v7
	v_exp_f32_e32 v8, v8
	v_rcp_f32_e32 v5, v5
	v_rcp_f32_e32 v6, v6
	v_add_f32_e32 v7, 1.0, v7
	v_add_f32_e32 v8, 1.0, v8
	v_rcp_f32_e32 v7, v7
	v_rcp_f32_e32 v8, v8
	v_fmamk_f32 v5, v5, 0x437f0000, v196
	v_fmamk_f32 v6, v6, 0x437f0000, v196
	v_fmamk_f32 v7, v7, 0x437f0000, v196
	v_fmamk_f32 v8, v8, 0x437f0000, v196
	v_perm_b32 v5, v6, v5, s67
	v_perm_b32 v6, v8, v7, s67
	v_mul_f32_e32 v7, 0xbcb8aa3b, v54
	v_mul_f32_e32 v8, 0xbcb8aa3b, v55
	v_exp_f32_e32 v7, v7
	v_exp_f32_e32 v8, v8
	v_perm_b32 v5, v6, v5, s68
	v_add_f32_e32 v6, 1.0, v7
	v_add_f32_e32 v7, 1.0, v8
	v_mul_f32_e32 v8, 0xbcb8aa3b, v56
	v_mul_f32_e32 v9, 0xbcb8aa3b, v57
	v_exp_f32_e32 v8, v8
	v_exp_f32_e32 v9, v9
	v_rcp_f32_e32 v6, v6
	v_rcp_f32_e32 v7, v7
	v_add_f32_e32 v8, 1.0, v8
	v_add_f32_e32 v9, 1.0, v9
	v_rcp_f32_e32 v8, v8
	v_rcp_f32_e32 v9, v9
	v_fmamk_f32 v6, v6, 0x437f0000, v196
	v_fmamk_f32 v7, v7, 0x437f0000, v196
	v_fmamk_f32 v8, v8, 0x437f0000, v196
	v_fmamk_f32 v9, v9, 0x437f0000, v196
	v_perm_b32 v6, v7, v6, s67
	v_perm_b32 v7, v9, v8, s67
	v_mul_f32_e32 v8, 0xbcb8aa3b, v50
	v_mul_f32_e32 v9, 0xbcb8aa3b, v51
	v_exp_f32_e32 v8, v8
	v_exp_f32_e32 v9, v9
	v_perm_b32 v6, v7, v6, s68
	v_add_f32_e32 v7, 1.0, v8
	v_add_f32_e32 v8, 1.0, v9
	v_mul_f32_e32 v9, 0xbcb8aa3b, v52
	v_mul_f32_e32 v10, 0xbcb8aa3b, v53
	v_exp_f32_e32 v9, v9
	v_exp_f32_e32 v10, v10
	v_rcp_f32_e32 v7, v7
	v_rcp_f32_e32 v8, v8
	v_add_f32_e32 v9, 1.0, v9
	v_add_f32_e32 v10, 1.0, v10
	v_rcp_f32_e32 v9, v9
	v_rcp_f32_e32 v10, v10
	v_fmamk_f32 v7, v7, 0x437f0000, v196
	v_fmamk_f32 v8, v8, 0x437f0000, v196
	v_fmamk_f32 v9, v9, 0x437f0000, v196
	v_fmamk_f32 v10, v10, 0x437f0000, v196
	v_perm_b32 v7, v8, v7, s67
	v_perm_b32 v8, v10, v9, s67
	v_perm_b32 v7, v8, v7, s68
	v_add_co_u32_e32 v8, vcc, s71, v2
	s_nop 0
	s_nop 0
	v_addc_co_u32_e32 v9, vcc, 0, v3, vcc
	global_store_dwordx4 v[8:9], v[4:7], off
	v_mul_f32_e32 v10, 0xbcb8aa3b, v46
	v_mul_f32_e32 v11, 0xbcb8aa3b, v47
	v_mul_f32_e32 v6, 0xbcb8aa3b, v48
	v_mul_f32_e32 v7, 0xbcb8aa3b, v49
	v_exp_f32_e32 v10, v10
	v_exp_f32_e32 v11, v11
	v_exp_f32_e32 v6, v6
	v_exp_f32_e32 v7, v7
	v_add_f32_e32 v4, 1.0, v10
	v_add_f32_e32 v5, 1.0, v11
	v_add_f32_e32 v6, 1.0, v6
	v_add_f32_e32 v7, 1.0, v7
	v_rcp_f32_e32 v4, v4
	v_rcp_f32_e32 v5, v5
	v_rcp_f32_e32 v6, v6
	v_rcp_f32_e32 v7, v7
	v_fmamk_f32 v4, v4, 0x437f0000, v196
	v_fmamk_f32 v5, v5, 0x437f0000, v196
	v_fmamk_f32 v6, v6, 0x437f0000, v196
	v_fmamk_f32 v7, v7, 0x437f0000, v196
	v_perm_b32 v4, v5, v4, s67
	v_perm_b32 v5, v7, v6, s67
	v_mul_f32_e32 v6, 0xbcb8aa3b, v42
	v_mul_f32_e32 v7, 0xbcb8aa3b, v43
	v_exp_f32_e32 v6, v6
	v_exp_f32_e32 v7, v7
	v_perm_b32 v4, v5, v4, s68
	v_add_f32_e32 v5, 1.0, v6
	v_add_f32_e32 v6, 1.0, v7
	v_mul_f32_e32 v7, 0xbcb8aa3b, v44
	v_mul_f32_e32 v8, 0xbcb8aa3b, v45
	v_exp_f32_e32 v7, v7
	v_exp_f32_e32 v8, v8
	v_rcp_f32_e32 v5, v5
	v_rcp_f32_e32 v6, v6
	v_add_f32_e32 v7, 1.0, v7
	v_add_f32_e32 v8, 1.0, v8
	v_rcp_f32_e32 v7, v7
	v_rcp_f32_e32 v8, v8
	v_fmamk_f32 v5, v5, 0x437f0000, v196
	v_fmamk_f32 v6, v6, 0x437f0000, v196
	v_fmamk_f32 v7, v7, 0x437f0000, v196
	v_fmamk_f32 v8, v8, 0x437f0000, v196
	v_perm_b32 v5, v6, v5, s67
	v_perm_b32 v6, v8, v7, s67
	v_mul_f32_e32 v7, 0xbcb8aa3b, v38
	v_mul_f32_e32 v8, 0xbcb8aa3b, v39
	v_exp_f32_e32 v7, v7
	v_exp_f32_e32 v8, v8
	v_perm_b32 v5, v6, v5, s68
	v_add_f32_e32 v6, 1.0, v7
	v_add_f32_e32 v7, 1.0, v8
	v_mul_f32_e32 v8, 0xbcb8aa3b, v40
	v_mul_f32_e32 v9, 0xbcb8aa3b, v41
	v_exp_f32_e32 v8, v8
	v_exp_f32_e32 v9, v9
	v_rcp_f32_e32 v6, v6
	v_rcp_f32_e32 v7, v7
	v_add_f32_e32 v8, 1.0, v8
	v_add_f32_e32 v9, 1.0, v9
	v_rcp_f32_e32 v8, v8
	v_rcp_f32_e32 v9, v9
	v_fmamk_f32 v6, v6, 0x437f0000, v196
	v_fmamk_f32 v7, v7, 0x437f0000, v196
	v_fmamk_f32 v8, v8, 0x437f0000, v196
	v_fmamk_f32 v9, v9, 0x437f0000, v196
	v_perm_b32 v6, v7, v6, s67
	v_perm_b32 v7, v9, v8, s67
	v_mul_f32_e32 v8, 0xbcb8aa3b, v34
	v_mul_f32_e32 v9, 0xbcb8aa3b, v35
	v_exp_f32_e32 v8, v8
	v_exp_f32_e32 v9, v9
	v_perm_b32 v6, v7, v6, s68
	v_add_f32_e32 v7, 1.0, v8
	v_add_f32_e32 v8, 1.0, v9
	v_mul_f32_e32 v9, 0xbcb8aa3b, v36
	v_mul_f32_e32 v10, 0xbcb8aa3b, v37
	v_exp_f32_e32 v9, v9
	v_exp_f32_e32 v10, v10
	v_rcp_f32_e32 v7, v7
	v_rcp_f32_e32 v8, v8
	v_add_f32_e32 v9, 1.0, v9
	v_add_f32_e32 v10, 1.0, v10
	v_rcp_f32_e32 v9, v9
	v_rcp_f32_e32 v10, v10
	v_fmamk_f32 v7, v7, 0x437f0000, v196
	v_fmamk_f32 v8, v8, 0x437f0000, v196
	v_fmamk_f32 v9, v9, 0x437f0000, v196
	v_fmamk_f32 v10, v10, 0x437f0000, v196
	v_add_co_u32_e32 v2, vcc, 0x58000, v2
	v_perm_b32 v7, v8, v7, s67
	v_perm_b32 v8, v10, v9, s67
	v_addc_co_u32_e32 v3, vcc, 0, v3, vcc
	v_perm_b32 v7, v8, v7, s68
	s_andn2_b64 vcc, exec, s[0:1]
	s_mov_b64 s[0:1], -1
	global_store_dwordx4 v[2:3], v[4:7], off
	s_cbranch_vccnz .LBB0_420
	s_andn2_b64 vcc, exec, s[10:11]
	s_cbranch_vccnz .LBB0_419
	s_branch .LBB0_419

; __device__ __forceinline__ f32x4 u8x4_f32(unsigned w) { return (f32x4){(float)(w & 0xffu), (float)((w >> 8) & 0xffu), (float)((w >> 16) & 0xffu), (float)(w >> 24)}; }
; __device__ __forceinline__ unsigned pk4_fp8(float a, float b, float c, float d) { int w = 0; w = __builtin_amdgcn_cvt_pk_fp8_f32(clamp8(a), clamp8(b), w, false); w = __builtin_amdgcn_cvt_pk_fp8_f32(clamp8(c), clamp8(d), w, true); return (unsigned)w; }
;     __device__ __forceinline__ void operator()(f32x4 (&acc)[2][2][4][2], const GUnit& u, int wr, int wc, int fr, int fq) const {
;         const size_t off0 = (size_t)(u.x0 * 256 + wr * 64 + fr) * D + u.x1 * 256 + wc * 64 + 16 * fq;
;         if (u.x2 == 0) {
; #pragma unroll
;             for (int ai = 0; ai < 2; ++ai) {
;                 u32x4 qs[4], qf[4];
; #pragma unroll
;                 for (int m = 0; m < 4; ++m) { const size_t off = off0 + (size_t)(ai * 128 + m * 16) * D; qs[m] = __builtin_nontemporal_load((const u32x4*)(GZS + off)); qf[m] = *(const u32x4*)(GZF + off); }
; #pragma unroll
;                 for (int m = 0; m < 4; ++m)
; #pragma unroll
;                     for (int q = 0; q < 4; ++q) { const f32x4 s = u8x4_f32(qs[m][q]), f = u8x4_f32(qf[m][q]); f32x4 r;
; #pragma unroll
;                         for (int j = 0; j < 4; ++j) r[j] = s[j] * S8_INV * __builtin_amdgcn_rcpf(fmaxf(f[j], 0.5f));
;                         acc[ai][q >> 1][m][q & 1] *= r; }
;                 asm volatile("" ::: "memory");
;             }
;             return;
;         }
; #pragma unroll
;         for (int ai = 0; ai < 2; ++ai) {
;             u32x4 qf[4];
; #pragma unroll
;             for (int m = 0; m < 4; ++m) qf[m] = __builtin_nontemporal_load((const u32x4*)(GZF + off0 + (size_t)(ai * 128 + m * 16) * D));
; #pragma unroll
;             for (int m = 0; m < 4; ++m) { u32x4 w;
; #pragma unroll
;                 for (int q = 0; q < 4; ++q) { const f32x4 f = u8x4_f32(qf[m][q]); const f32x4 a = acc[ai][q >> 1][m][q & 1]; f32x4 v;
; #pragma unroll
;                     for (int j = 0; j < 4; ++j) v[j] = a[j] * (fmaxf(f[j], 0.5f) * (W8_INV / 255.0f));
;                     w[q] = pk4_fp8(v[0], v[1], v[2], v[3]); }
;                 *(u32x4*)(M8 + tiled_off((size_t)(u.x0 * 256 + wr * 64 + fr + ai * 128 + m * 16), u.x1 * 256 + wc * 64 + 16 * fq, D / 128)) = w; }
;             asm volatile("" ::: "memory");
;         }
;     }
.LBB0_837:
	s_lshl_b32 s28, s71, 8
	v_add_u32_e32 v144, s28, v177
	v_ashrrev_i32_e32 v145, 31, v144
	s_lshl_b32 s26, s70, 8
	v_lshlrev_b64 v[2:3], 11, v[144:145]
	s_ashr_i32 s27, s26, 31
	v_lshl_add_u64 v[142:143], v[2:3], 0, s[26:27]
	v_or_b32_e32 v142, v142, v176
	s_cmp_lg_u32 s73, 0
	s_cselect_b64 s[24:25], -1, 0
	s_cmp_eq_u32 s73, 0
	v_lshl_add_u64 v[12:13], s[6:7], 0, v[142:143]
	s_nop 15
	s_nop 7
	s_cbranch_scc1 .LBB0_845
	global_load_dwordx4 v[146:149], v[12:13], off nt
	v_add_co_u32_e32 v2, vcc, 0x8000, v12
	v_mov_b32_e32 v151, 0
	s_nop 0
	v_addc_co_u32_e32 v3, vcc, 0, v13, vcc
	v_add_co_u32_e32 v4, vcc, 0x10000, v12
	v_mov_b32_e32 v150, 0
	s_nop 0
	v_addc_co_u32_e32 v5, vcc, 0, v13, vcc
	global_load_dwordx4 v[154:157], v[2:3], off nt
	global_load_dwordx4 v[6:9], v[4:5], off nt
	v_add_co_u32_e32 v188, vcc, 0x18000, v12
	v_mov_b32_e32 v152, 0
	s_nop 0
	v_addc_co_u32_e32 v189, vcc, 0, v13, vcc
	global_load_dwordx4 v[2:5], v[188:189], off nt
	s_or_b32 s26, s26, s53
	s_ashr_i32 s26, s26, 7
	s_ashr_i32 s27, s26, 31
	s_waitcnt vmcnt(0) lgkmcnt(0)
	v_cvt_f32_ubyte0_e32 v189, v147
	v_cvt_f32_ubyte1_e32 v201, v147
	v_max_f32_e32 v189, 0.5, v189
	v_max_f32_e32 v201, 0.5, v201
	v_mul_f32_e32 v189, 0x38808081, v189
	v_mul_f32_e32 v201, 0x38808081, v201
	v_cvt_f32_ubyte0_e32 v10, v146
	v_cvt_f32_ubyte1_e32 v153, v146
	v_cvt_f32_ubyte0_e32 v203, v148
	v_cvt_f32_ubyte1_e32 v204, v148
	v_mul_f32_e32 v189, v134, v189
	v_mul_f32_e32 v201, v135, v201
	v_cvt_f32_ubyte2_e32 v202, v147
	v_cvt_f32_ubyte3_e32 v147, v147
	v_max_f32_e32 v10, 0.5, v10
	v_max_f32_e32 v153, 0.5, v153
	v_max_f32_e32 v203, 0.5, v203
	v_max_f32_e32 v204, 0.5, v204
	v_med3_f32 v189, v189, s60, v200
	v_med3_f32 v201, v201, s60, v200
	v_cvt_f32_ubyte2_e32 v205, v148
	v_cvt_f32_ubyte3_e32 v148, v148
	v_max_f32_e32 v202, 0.5, v202
	v_max_f32_e32 v147, 0.5, v147
	v_mul_f32_e32 v10, 0x38808081, v10
	v_mul_f32_e32 v153, 0x38808081, v153
	v_mul_f32_e32 v203, 0x38808081, v203
	v_mul_f32_e32 v204, 0x38808081, v204
	v_cvt_pk_fp8_f32 v151, v189, v201
	v_max_f32_e32 v148, 0.5, v148
	v_mul_f32_e32 v202, 0x38808081, v202
	v_mul_f32_e32 v147, 0x38808081, v147
	v_mul_f32_e32 v10, v138, v10
	v_mul_f32_e32 v153, v139, v153
	v_mul_f32_e32 v203, v106, v203
	v_mul_f32_e32 v204, v107, v204
	v_cvt_f32_ubyte2_e32 v188, v146
	v_cvt_f32_ubyte3_e32 v146, v146
	v_mul_f32_e32 v148, 0x38808081, v148
	v_mul_f32_e32 v202, v136, v202
	v_mul_f32_e32 v147, v137, v147
	v_med3_f32 v10, v10, s60, v200
	v_med3_f32 v153, v153, s60, v200
	v_med3_f32 v203, v203, s60, v200
	v_med3_f32 v204, v204, s60, v200
	v_cvt_f32_ubyte0_e32 v206, v149
	v_cvt_f32_ubyte1_e32 v207, v149
	v_max_f32_e32 v188, 0.5, v188
	v_max_f32_e32 v146, 0.5, v146
	v_max_f32_e32 v205, 0.5, v205
	v_mul_f32_e32 v148, v109, v148
	v_med3_f32 v202, v202, s60, v200
	v_med3_f32 v147, v147, s60, v200
	v_cvt_pk_fp8_f32 v150, v10, v153
	v_cvt_pk_fp8_f32 v152, v203, v204
	v_mul_f32_e32 v188, 0x38808081, v188
	v_mul_f32_e32 v146, 0x38808081, v146
	v_mul_f32_e32 v205, 0x38808081, v205
	v_med3_f32 v10, v148, s60, v200
	v_cvt_pk_fp8_f32 v151, v202, v147 op_sel:[0,0,1]
	v_max_f32_e32 v147, 0.5, v206
	v_max_f32_e32 v148, 0.5, v207
	v_mul_f32_e32 v188, v140, v188
	v_mul_f32_e32 v146, v141, v146
	v_mul_f32_e32 v205, v108, v205
	v_mul_f32_e32 v147, 0x38808081, v147
	v_mul_f32_e32 v148, 0x38808081, v148
	v_med3_f32 v188, v188, s60, v200
	v_med3_f32 v146, v146, s60, v200
	v_med3_f32 v205, v205, s60, v200
	v_mul_f32_e32 v147, v102, v147
	v_mul_f32_e32 v148, v103, v148
	v_cvt_pk_fp8_f32 v150, v188, v146 op_sel:[0,0,1]
	v_cvt_pk_fp8_f32 v152, v205, v10 op_sel:[0,0,1]
	v_cvt_f32_ubyte2_e32 v10, v149
	v_cvt_f32_ubyte3_e32 v146, v149
	v_med3_f32 v147, v147, s60, v200
	v_med3_f32 v148, v148, s60, v200
	v_mov_b32_e32 v153, 0
	v_max_f32_e32 v10, 0.5, v10
	v_max_f32_e32 v146, 0.5, v146
	v_cvt_pk_fp8_f32 v153, v147, v148
	v_mul_f32_e32 v10, 0x38808081, v10
	v_mul_f32_e32 v146, 0x38808081, v146
	v_mul_f32_e32 v10, v104, v10
	v_mul_f32_e32 v146, v105, v146
	v_med3_f32 v10, v10, s60, v200
	v_med3_f32 v146, v146, s60, v200
	v_cvt_pk_fp8_f32 v153, v10, v146 op_sel:[0,0,1]
	v_lshrrev_b64 v[146:147], 4, v[144:145]
	v_and_b32_e32 v147, 0x1ffff, v147
	v_and_b32_e32 v146, -16, v146
	v_lshl_add_u64 v[146:147], v[146:147], 0, s[26:27]
	v_lshlrev_b64 v[146:147], 15, v[146:147]
	v_lshlrev_b32_e32 v10, 7, v144
	v_and_b32_e32 v10, 0x6780, v10
	v_lshl_add_u64 v[144:145], s[12:13], 0, v[146:147]
	v_lshl_add_u64 v[144:145], v[144:145], 0, v[10:11]
	v_lshl_add_u64 v[144:145], v[144:145], 0, v[178:179]
	global_store_dwordx4 v[144:145], v[150:153], off
	v_cvt_f32_ubyte0_e32 v10, v154
	v_cvt_f32_ubyte1_e32 v144, v154
	v_max_f32_e32 v10, 0.5, v10
	v_max_f32_e32 v144, 0.5, v144
	v_mul_f32_e32 v10, 0x38808081, v10
	v_mul_f32_e32 v144, 0x38808081, v144
	v_mul_f32_e32 v10, v130, v10
	v_mul_f32_e32 v144, v131, v144
	v_cvt_f32_ubyte2_e32 v145, v154
	v_cvt_f32_ubyte3_e32 v146, v154
	v_med3_f32 v10, v10, s60, v200
	v_med3_f32 v147, v144, s60, v200
	v_mov_b32_e32 v144, v11
	v_max_f32_e32 v145, 0.5, v145
	v_max_f32_e32 v146, 0.5, v146
	v_cvt_pk_fp8_f32 v144, v10, v147
	v_mul_f32_e32 v145, 0x38808081, v145
	v_mul_f32_e32 v146, 0x38808081, v146
	v_mul_f32_e32 v145, v132, v145
	v_mul_f32_e32 v10, v133, v146
	v_med3_f32 v145, v145, s60, v200
	v_med3_f32 v10, v10, s60, v200
	v_cvt_pk_fp8_f32 v144, v145, v10 op_sel:[0,0,1]
	v_cvt_f32_ubyte0_e32 v10, v155
	v_cvt_f32_ubyte1_e32 v145, v155
	v_max_f32_e32 v10, 0.5, v10
	v_max_f32_e32 v145, 0.5, v145
	v_mul_f32_e32 v10, 0x38808081, v10
	v_mul_f32_e32 v145, 0x38808081, v145
	v_mul_f32_e32 v10, v126, v10
	v_mul_f32_e32 v145, v127, v145
	v_cvt_f32_ubyte2_e32 v146, v155
; __device__ __forceinline__ f32x4 u8x4_f32(unsigned w) { return (f32x4){(float)(w & 0xffu), (float)((w >> 8) & 0xffu), (float)((w >> 16) & 0xffu), (float)(w >> 24)}; }
; __device__ __forceinline__ unsigned pk4_fp8(float a, float b, float c, float d) { int w = 0; w = __builtin_amdgcn_cvt_pk_fp8_f32(clamp8(a), clamp8(b), w, false); w = __builtin_amdgcn_cvt_pk_fp8_f32(clamp8(c), clamp8(d), w, true); return (unsigned)w; }
; __host__ __device__ __forceinline__ size_t tiled_off(size_t r, int kb, int ktiles) { return (((r >> 8) * ktiles + (kb >> 7)) << 15) + ((r & 255) << 7) + (kb & 127); }
;     __device__ __forceinline__ void operator()(f32x4 (&acc)[2][2][4][2], const GUnit& u, int wr, int wc, int fr, int fq) const {
;     ...
;             for (int m = 0; m < 4; ++m) qf[m] = __builtin_nontemporal_load((const u32x4*)(GZF + off0 + (size_t)(ai * 128 + m * 16) * D));
; #pragma unroll
;             for (int m = 0; m < 4; ++m) { u32x4 w;
; #pragma unroll
;                 for (int q = 0; q < 4; ++q) { const f32x4 f = u8x4_f32(qf[m][q]); const f32x4 a = acc[ai][q >> 1][m][q & 1]; f32x4 v;
; #pragma unroll
;                     for (int j = 0; j < 4; ++j) v[j] = a[j] * (fmaxf(f[j], 0.5f) * (W8_INV / 255.0f));
;                     w[q] = pk4_fp8(v[0], v[1], v[2], v[3]); }
;                 *(u32x4*)(M8 + tiled_off((size_t)(u.x0 * 256 + wr * 64 + fr + ai * 128 + m * 16), u.x1 * 256 + wc * 64 + 16 * fq, D / 128)) = w; }
;             asm volatile("" ::: "memory");
;         }
;     }
	v_cvt_f32_ubyte3_e32 v147, v155
	v_med3_f32 v10, v10, s60, v200
	v_med3_f32 v148, v145, s60, v200
	v_mov_b32_e32 v145, v11
	v_max_f32_e32 v146, 0.5, v146
	v_max_f32_e32 v147, 0.5, v147
	v_cvt_pk_fp8_f32 v145, v10, v148
	v_mul_f32_e32 v146, 0x38808081, v146
	v_mul_f32_e32 v147, 0x38808081, v147
	v_mul_f32_e32 v146, v128, v146
	v_mul_f32_e32 v10, v129, v147
	v_med3_f32 v146, v146, s60, v200
	v_med3_f32 v10, v10, s60, v200
	v_cvt_pk_fp8_f32 v145, v146, v10 op_sel:[0,0,1]
	v_cvt_f32_ubyte0_e32 v10, v156
	v_cvt_f32_ubyte1_e32 v146, v156
	v_max_f32_e32 v10, 0.5, v10
	v_max_f32_e32 v146, 0.5, v146
	v_mul_f32_e32 v10, 0x38808081, v10
	v_mul_f32_e32 v146, 0x38808081, v146
	v_mul_f32_e32 v10, v98, v10
	v_mul_f32_e32 v146, v99, v146
	v_cvt_f32_ubyte2_e32 v147, v156
	v_cvt_f32_ubyte3_e32 v148, v156
	v_med3_f32 v10, v10, s60, v200
	v_med3_f32 v149, v146, s60, v200
	v_mov_b32_e32 v146, v11
	v_max_f32_e32 v147, 0.5, v147
	v_max_f32_e32 v148, 0.5, v148
	v_cvt_pk_fp8_f32 v146, v10, v149
	v_mul_f32_e32 v147, 0x38808081, v147
	v_mul_f32_e32 v148, 0x38808081, v148
	v_mul_f32_e32 v147, v100, v147
	v_mul_f32_e32 v10, v101, v148
	v_med3_f32 v147, v147, s60, v200
	v_med3_f32 v10, v10, s60, v200
	v_cvt_pk_fp8_f32 v146, v147, v10 op_sel:[0,0,1]
	v_cvt_f32_ubyte0_e32 v10, v157
	v_cvt_f32_ubyte1_e32 v147, v157
	v_max_f32_e32 v10, 0.5, v10
	v_max_f32_e32 v147, 0.5, v147
	v_mul_f32_e32 v10, 0x38808081, v10
	v_mul_f32_e32 v147, 0x38808081, v147
	v_mul_f32_e32 v10, v94, v10
	v_mul_f32_e32 v147, v95, v147
	v_cvt_f32_ubyte2_e32 v148, v157
	v_cvt_f32_ubyte3_e32 v149, v157
	v_med3_f32 v10, v10, s60, v200
	v_med3_f32 v150, v147, s60, v200
	v_mov_b32_e32 v147, v11
	v_max_f32_e32 v148, 0.5, v148
	v_max_f32_e32 v149, 0.5, v149
	v_cvt_pk_fp8_f32 v147, v10, v150
	v_mul_f32_e32 v148, 0x38808081, v148
	v_mul_f32_e32 v149, 0x38808081, v149
	v_mul_f32_e32 v148, v96, v148
	v_mul_f32_e32 v10, v97, v149
	v_med3_f32 v148, v148, s60, v200
	v_med3_f32 v10, v10, s60, v200
	v_cvt_pk_fp8_f32 v147, v148, v10 op_sel:[0,0,1]
	v_add_u32_e32 v148, s28, v191
	v_ashrrev_i32_e32 v149, 31, v148
	v_lshrrev_b64 v[150:151], 4, v[148:149]
	v_and_b32_e32 v151, 0x1ffff, v151
	v_and_b32_e32 v150, -16, v150
	v_lshl_add_u64 v[150:151], v[150:151], 0, s[26:27]
	v_lshlrev_b64 v[150:151], 15, v[150:151]
	v_lshlrev_b32_e32 v10, 7, v148
	v_and_b32_e32 v10, 0x7f80, v10
	v_lshl_add_u64 v[148:149], s[12:13], 0, v[150:151]
	v_lshl_add_u64 v[148:149], v[148:149], 0, v[10:11]
	v_lshl_add_u64 v[148:149], v[148:149], 0, v[178:179]
	global_store_dwordx4 v[148:149], v[144:147], off
	v_cvt_f32_ubyte0_e32 v10, v6
	v_max_f32_e32 v10, 0.5, v10
	v_cvt_f32_ubyte1_e32 v144, v6
	v_max_f32_e32 v144, 0.5, v144
	v_cvt_f32_ubyte2_e32 v145, v6
	v_cvt_f32_ubyte3_e32 v6, v6
	v_mul_f32_e32 v10, 0x38808081, v10
	v_mul_f32_e32 v144, 0x38808081, v144
	v_mul_f32_e32 v10, v122, v10
	v_mul_f32_e32 v144, v123, v144
	v_max_f32_e32 v6, 0.5, v6
	v_mul_f32_e32 v146, 0x38808081, v6
	v_med3_f32 v10, v10, s60, v200
	v_med3_f32 v144, v144, s60, v200
	v_mov_b32_e32 v6, v11
	v_max_f32_e32 v145, 0.5, v145
	v_cvt_pk_fp8_f32 v6, v10, v144
	v_mul_f32_e32 v145, 0x38808081, v145
	v_mul_f32_e32 v145, v124, v145
	v_mul_f32_e32 v10, v125, v146
	v_med3_f32 v144, v145, s60, v200
	v_med3_f32 v10, v10, s60, v200
	v_cvt_pk_fp8_f32 v6, v144, v10 op_sel:[0,0,1]
	v_cvt_f32_ubyte0_e32 v10, v7
	v_cvt_f32_ubyte1_e32 v144, v7
	v_max_f32_e32 v10, 0.5, v10
	v_max_f32_e32 v144, 0.5, v144
	v_cvt_f32_ubyte2_e32 v145, v7
	v_cvt_f32_ubyte3_e32 v7, v7
	v_mul_f32_e32 v10, 0x38808081, v10
	v_mul_f32_e32 v144, 0x38808081, v144
	v_mul_f32_e32 v10, v118, v10
	v_mul_f32_e32 v144, v119, v144
	v_max_f32_e32 v7, 0.5, v7
	v_mul_f32_e32 v146, 0x38808081, v7
	v_med3_f32 v10, v10, s60, v200
	v_med3_f32 v144, v144, s60, v200
	v_mov_b32_e32 v7, v11
	v_max_f32_e32 v145, 0.5, v145
	v_cvt_pk_fp8_f32 v7, v10, v144
	v_mul_f32_e32 v145, 0x38808081, v145
	v_mul_f32_e32 v145, v120, v145
	v_mul_f32_e32 v10, v121, v146
	v_med3_f32 v144, v145, s60, v200
	v_med3_f32 v10, v10, s60, v200
	v_cvt_pk_fp8_f32 v7, v144, v10 op_sel:[0,0,1]
	v_cvt_f32_ubyte0_e32 v10, v8
	v_cvt_f32_ubyte1_e32 v144, v8
	v_max_f32_e32 v10, 0.5, v10
	v_max_f32_e32 v144, 0.5, v144
	v_cvt_f32_ubyte2_e32 v145, v8
	v_cvt_f32_ubyte3_e32 v8, v8
	v_mul_f32_e32 v10, 0x38808081, v10
	v_mul_f32_e32 v144, 0x38808081, v144
	v_mul_f32_e32 v10, v90, v10
	v_mul_f32_e32 v144, v91, v144
	v_max_f32_e32 v8, 0.5, v8
	v_mul_f32_e32 v146, 0x38808081, v8
	v_med3_f32 v10, v10, s60, v200
	v_med3_f32 v144, v144, s60, v200
	v_mov_b32_e32 v8, v11
	v_max_f32_e32 v145, 0.5, v145
	v_cvt_pk_fp8_f32 v8, v10, v144
	v_mul_f32_e32 v145, 0x38808081, v145
	v_mul_f32_e32 v145, v92, v145
	v_mul_f32_e32 v10, v93, v146
	v_med3_f32 v144, v145, s60, v200
	v_med3_f32 v10, v10, s60, v200
	v_cvt_pk_fp8_f32 v8, v144, v10 op_sel:[0,0,1]
	v_cvt_f32_ubyte0_e32 v10, v9
	v_cvt_f32_ubyte1_e32 v144, v9
	v_max_f32_e32 v10, 0.5, v10
	v_max_f32_e32 v144, 0.5, v144
	v_cvt_f32_ubyte2_e32 v145, v9
	v_cvt_f32_ubyte3_e32 v9, v9
	v_mul_f32_e32 v10, 0x38808081, v10
	v_mul_f32_e32 v144, 0x38808081, v144
	v_mul_f32_e32 v10, v86, v10
	v_mul_f32_e32 v144, v87, v144
	v_max_f32_e32 v9, 0.5, v9
	v_mul_f32_e32 v146, 0x38808081, v9
	v_med3_f32 v10, v10, s60, v200
	v_med3_f32 v144, v144, s60, v200
	v_mov_b32_e32 v9, v11
	v_max_f32_e32 v145, 0.5, v145
	v_cvt_pk_fp8_f32 v9, v10, v144
	v_mul_f32_e32 v145, 0x38808081, v145
	v_mul_f32_e32 v145, v88, v145
	v_mul_f32_e32 v10, v89, v146
	v_med3_f32 v144, v145, s60, v200
	v_med3_f32 v10, v10, s60, v200
	v_cvt_pk_fp8_f32 v9, v144, v10 op_sel:[0,0,1]
	v_add_u32_e32 v144, s28, v192
	v_ashrrev_i32_e32 v145, 31, v144
	v_lshrrev_b64 v[146:147], 4, v[144:145]
; __device__ __forceinline__ f32x4 u8x4_f32(unsigned w) { return (f32x4){(float)(w & 0xffu), (float)((w >> 8) & 0xffu), (float)((w >> 16) & 0xffu), (float)(w >> 24)}; }
; __device__ __forceinline__ unsigned pk4_fp8(float a, float b, float c, float d) { int w = 0; w = __builtin_amdgcn_cvt_pk_fp8_f32(clamp8(a), clamp8(b), w, false); w = __builtin_amdgcn_cvt_pk_fp8_f32(clamp8(c), clamp8(d), w, true); return (unsigned)w; }
; __host__ __device__ __forceinline__ size_t tiled_off(size_t r, int kb, int ktiles) { return (((r >> 8) * ktiles + (kb >> 7)) << 15) + ((r & 255) << 7) + (kb & 127); }
;     __device__ __forceinline__ void operator()(f32x4 (&acc)[2][2][4][2], const GUnit& u, int wr, int wc, int fr, int fq) const {
;     ...
;             for (int m = 0; m < 4; ++m) qf[m] = __builtin_nontemporal_load((const u32x4*)(GZF + off0 + (size_t)(ai * 128 + m * 16) * D));
; #pragma unroll
;             for (int m = 0; m < 4; ++m) { u32x4 w;
; #pragma unroll
;                 for (int q = 0; q < 4; ++q) { const f32x4 f = u8x4_f32(qf[m][q]); const f32x4 a = acc[ai][q >> 1][m][q & 1]; f32x4 v;
; #pragma unroll
;                     for (int j = 0; j < 4; ++j) v[j] = a[j] * (fmaxf(f[j], 0.5f) * (W8_INV / 255.0f));
;                     w[q] = pk4_fp8(v[0], v[1], v[2], v[3]); }
;                 *(u32x4*)(M8 + tiled_off((size_t)(u.x0 * 256 + wr * 64 + fr + ai * 128 + m * 16), u.x1 * 256 + wc * 64 + 16 * fq, D / 128)) = w; }
;             asm volatile("" ::: "memory");
;         }
;     }
	v_and_b32_e32 v147, 0x1ffff, v147
	v_and_b32_e32 v146, -16, v146
	v_lshl_add_u64 v[146:147], v[146:147], 0, s[26:27]
	v_lshlrev_b64 v[146:147], 15, v[146:147]
	v_lshlrev_b32_e32 v10, 7, v144
	v_and_b32_e32 v10, 0x7f80, v10
	v_lshl_add_u64 v[144:145], s[12:13], 0, v[146:147]
	v_lshl_add_u64 v[144:145], v[144:145], 0, v[10:11]
	v_lshl_add_u64 v[144:145], v[144:145], 0, v[178:179]
	global_store_dwordx4 v[144:145], v[6:9], off
	s_nop 1
	v_cvt_f32_ubyte0_e32 v6, v2
	v_cvt_f32_ubyte1_e32 v7, v2
	v_max_f32_e32 v6, 0.5, v6
	v_max_f32_e32 v7, 0.5, v7
	v_cvt_f32_ubyte2_e32 v8, v2
	v_cvt_f32_ubyte3_e32 v2, v2
	v_mul_f32_e32 v6, 0x38808081, v6
	v_mul_f32_e32 v7, 0x38808081, v7
	v_mul_f32_e32 v6, v114, v6
	v_mul_f32_e32 v7, v115, v7
	v_max_f32_e32 v2, 0.5, v2
	v_mul_f32_e32 v9, 0x38808081, v2
	v_med3_f32 v6, v6, s60, v200
	v_med3_f32 v7, v7, s60, v200
	v_mov_b32_e32 v2, v11
	v_max_f32_e32 v8, 0.5, v8
	v_cvt_pk_fp8_f32 v2, v6, v7
	v_mul_f32_e32 v8, 0x38808081, v8
	v_mul_f32_e32 v8, v116, v8
	v_mul_f32_e32 v6, v117, v9
	v_med3_f32 v7, v8, s60, v200
	v_med3_f32 v6, v6, s60, v200
	v_cvt_pk_fp8_f32 v2, v7, v6 op_sel:[0,0,1]
	v_cvt_f32_ubyte0_e32 v6, v3
	v_cvt_f32_ubyte1_e32 v7, v3
	v_max_f32_e32 v6, 0.5, v6
	v_max_f32_e32 v7, 0.5, v7
	v_cvt_f32_ubyte2_e32 v8, v3
	v_cvt_f32_ubyte3_e32 v3, v3
	v_mul_f32_e32 v6, 0x38808081, v6
	v_mul_f32_e32 v7, 0x38808081, v7
	v_mul_f32_e32 v6, v110, v6
	v_mul_f32_e32 v7, v111, v7
	v_max_f32_e32 v3, 0.5, v3
	v_mul_f32_e32 v9, 0x38808081, v3
	v_med3_f32 v6, v6, s60, v200
	v_med3_f32 v7, v7, s60, v200
	v_mov_b32_e32 v3, v11
	v_max_f32_e32 v8, 0.5, v8
	v_cvt_pk_fp8_f32 v3, v6, v7
	v_mul_f32_e32 v8, 0x38808081, v8
	v_mul_f32_e32 v8, v112, v8
	v_mul_f32_e32 v6, v113, v9
	v_med3_f32 v7, v8, s60, v200
	v_med3_f32 v6, v6, s60, v200
	v_cvt_pk_fp8_f32 v3, v7, v6 op_sel:[0,0,1]
	v_cvt_f32_ubyte0_e32 v6, v4
	v_cvt_f32_ubyte1_e32 v7, v4
	v_max_f32_e32 v6, 0.5, v6
	v_max_f32_e32 v7, 0.5, v7
	v_cvt_f32_ubyte2_e32 v8, v4
	v_cvt_f32_ubyte3_e32 v4, v4
	v_mul_f32_e32 v6, 0x38808081, v6
	v_mul_f32_e32 v7, 0x38808081, v7
	v_mul_f32_e32 v6, v82, v6
	v_mul_f32_e32 v7, v83, v7
	v_max_f32_e32 v4, 0.5, v4
	v_mul_f32_e32 v9, 0x38808081, v4
	v_med3_f32 v6, v6, s60, v200
	v_med3_f32 v7, v7, s60, v200
	v_mov_b32_e32 v4, v11
	v_max_f32_e32 v8, 0.5, v8
	v_cvt_pk_fp8_f32 v4, v6, v7
	v_mul_f32_e32 v8, 0x38808081, v8
	v_mul_f32_e32 v8, v84, v8
	v_mul_f32_e32 v6, v85, v9
	v_med3_f32 v7, v8, s60, v200
	v_med3_f32 v6, v6, s60, v200
	v_cvt_pk_fp8_f32 v4, v7, v6 op_sel:[0,0,1]
	v_cvt_f32_ubyte0_e32 v6, v5
	v_cvt_f32_ubyte1_e32 v7, v5
	v_max_f32_e32 v6, 0.5, v6
	v_max_f32_e32 v7, 0.5, v7
	v_cvt_f32_ubyte2_e32 v8, v5
	v_cvt_f32_ubyte3_e32 v5, v5
	v_mul_f32_e32 v6, 0x38808081, v6
	v_mul_f32_e32 v7, 0x38808081, v7
	v_mul_f32_e32 v6, v78, v6
	v_mul_f32_e32 v7, v79, v7
	v_max_f32_e32 v5, 0.5, v5
	v_mul_f32_e32 v9, 0x38808081, v5
	v_med3_f32 v6, v6, s60, v200
	v_med3_f32 v7, v7, s60, v200
	v_mov_b32_e32 v5, v11
	v_max_f32_e32 v8, 0.5, v8
	v_cvt_pk_fp8_f32 v5, v6, v7
	v_mul_f32_e32 v8, 0x38808081, v8
	v_mul_f32_e32 v8, v80, v8
	v_mul_f32_e32 v6, v81, v9
	v_med3_f32 v7, v8, s60, v200
	v_med3_f32 v6, v6, s60, v200
	v_cvt_pk_fp8_f32 v5, v7, v6 op_sel:[0,0,1]
	v_add_u32_e32 v6, s28, v193
	v_ashrrev_i32_e32 v7, 31, v6
	v_lshrrev_b64 v[8:9], 4, v[6:7]
	v_and_b32_e32 v9, 0x1ffff, v9
	v_and_b32_e32 v8, -16, v8
	v_lshl_add_u64 v[8:9], v[8:9], 0, s[26:27]
	v_lshlrev_b64 v[8:9], 15, v[8:9]
	v_lshlrev_b32_e32 v6, 7, v6
	v_and_b32_e32 v10, 0x7f80, v6
	v_lshl_add_u64 v[6:7], s[12:13], 0, v[8:9]
	v_lshl_add_u64 v[6:7], v[6:7], 0, v[10:11]
	v_lshl_add_u64 v[6:7], v[6:7], 0, v[178:179]
	global_store_dwordx4 v[6:7], v[2:5], off
	s_nop 1
	v_add_co_u32_e32 v2, vcc, s61, v12
	s_nop 1
	v_addc_co_u32_e32 v3, vcc, 0, v13, vcc
	global_load_dwordx4 v[144:147], v[2:3], off nt
	v_add_co_u32_e32 v2, vcc, s62, v12
	s_waitcnt vmcnt(0) lgkmcnt(0)
	v_cvt_f32_ubyte0_e32 v10, v144
	v_addc_co_u32_e32 v3, vcc, 0, v13, vcc
	global_load_dwordx4 v[148:151], v[2:3], off nt
	v_cvt_f32_ubyte1_e32 v152, v144
	v_max_f32_e32 v10, 0.5, v10
	v_max_f32_e32 v152, 0.5, v152
	v_cvt_f32_ubyte2_e32 v153, v144
	v_cvt_f32_ubyte3_e32 v144, v144
	v_mul_f32_e32 v10, 0x38808081, v10
	v_mul_f32_e32 v152, 0x38808081, v152
	v_mul_f32_e32 v10, v74, v10
	v_mul_f32_e32 v152, v75, v152
	v_max_f32_e32 v144, 0.5, v144
	v_mul_f32_e32 v154, 0x38808081, v144
	v_med3_f32 v10, v10, s60, v200
	v_med3_f32 v152, v152, s60, v200
	v_mov_b32_e32 v144, v11
	v_max_f32_e32 v153, 0.5, v153
	v_cvt_pk_fp8_f32 v144, v10, v152
	v_mul_f32_e32 v153, 0x38808081, v153
	v_add_co_u32_e32 v2, vcc, s63, v12
	v_mul_f32_e32 v153, v76, v153
	v_mul_f32_e32 v10, v77, v154
	v_addc_co_u32_e32 v3, vcc, 0, v13, vcc
	v_med3_f32 v152, v153, s60, v200
	v_med3_f32 v10, v10, s60, v200
	v_add_co_u32_e32 v4, vcc, s64, v12
	v_cvt_pk_fp8_f32 v144, v152, v10 op_sel:[0,0,1]
	v_cvt_f32_ubyte0_e32 v10, v145
	v_cvt_f32_ubyte1_e32 v152, v145
	v_addc_co_u32_e32 v5, vcc, 0, v13, vcc
	v_max_f32_e32 v10, 0.5, v10
	v_max_f32_e32 v152, 0.5, v152
	global_load_dwordx4 v[6:9], v[2:3], off nt
	s_nop 0
	global_load_dwordx4 v[2:5], v[4:5], off nt
	v_cvt_f32_ubyte2_e32 v153, v145
	v_cvt_f32_ubyte3_e32 v145, v145
	v_mul_f32_e32 v10, 0x38808081, v10
	v_mul_f32_e32 v152, 0x38808081, v152
	v_mul_f32_e32 v10, v70, v10
	v_mul_f32_e32 v152, v71, v152
	v_max_f32_e32 v145, 0.5, v145
	v_mul_f32_e32 v154, 0x38808081, v145
	v_med3_f32 v10, v10, s60, v200
	v_med3_f32 v152, v152, s60, v200
	v_mov_b32_e32 v145, v11
	v_max_f32_e32 v153, 0.5, v153
	v_cvt_pk_fp8_f32 v145, v10, v152
	v_mul_f32_e32 v153, 0x38808081, v153
	v_mul_f32_e32 v153, v72, v153
	v_mul_f32_e32 v10, v73, v154
	v_med3_f32 v152, v153, s60, v200
; __device__ __forceinline__ f32x4 u8x4_f32(unsigned w) { return (f32x4){(float)(w & 0xffu), (float)((w >> 8) & 0xffu), (float)((w >> 16) & 0xffu), (float)(w >> 24)}; }
; __device__ __forceinline__ unsigned pk4_fp8(float a, float b, float c, float d) { int w = 0; w = __builtin_amdgcn_cvt_pk_fp8_f32(clamp8(a), clamp8(b), w, false); w = __builtin_amdgcn_cvt_pk_fp8_f32(clamp8(c), clamp8(d), w, true); return (unsigned)w; }
; __host__ __device__ __forceinline__ size_t tiled_off(size_t r, int kb, int ktiles) { return (((r >> 8) * ktiles + (kb >> 7)) << 15) + ((r & 255) << 7) + (kb & 127); }
;     __device__ __forceinline__ void operator()(f32x4 (&acc)[2][2][4][2], const GUnit& u, int wr, int wc, int fr, int fq) const {
;     ...
;             for (int m = 0; m < 4; ++m) qf[m] = __builtin_nontemporal_load((const u32x4*)(GZF + off0 + (size_t)(ai * 128 + m * 16) * D));
; #pragma unroll
;             for (int m = 0; m < 4; ++m) { u32x4 w;
; #pragma unroll
;                 for (int q = 0; q < 4; ++q) { const f32x4 f = u8x4_f32(qf[m][q]); const f32x4 a = acc[ai][q >> 1][m][q & 1]; f32x4 v;
; #pragma unroll
;                     for (int j = 0; j < 4; ++j) v[j] = a[j] * (fmaxf(f[j], 0.5f) * (W8_INV / 255.0f));
;                     w[q] = pk4_fp8(v[0], v[1], v[2], v[3]); }
;                 *(u32x4*)(M8 + tiled_off((size_t)(u.x0 * 256 + wr * 64 + fr + ai * 128 + m * 16), u.x1 * 256 + wc * 64 + 16 * fq, D / 128)) = w; }
;             asm volatile("" ::: "memory");
;         }
;     }
	v_med3_f32 v10, v10, s60, v200
	v_cvt_pk_fp8_f32 v145, v152, v10 op_sel:[0,0,1]
	v_cvt_f32_ubyte0_e32 v10, v146
	v_cvt_f32_ubyte1_e32 v152, v146
	v_max_f32_e32 v10, 0.5, v10
	v_max_f32_e32 v152, 0.5, v152
	v_cvt_f32_ubyte2_e32 v153, v146
	v_cvt_f32_ubyte3_e32 v146, v146
	v_mul_f32_e32 v10, 0x38808081, v10
	v_mul_f32_e32 v152, 0x38808081, v152
	v_mul_f32_e32 v10, v42, v10
	v_mul_f32_e32 v152, v43, v152
	v_max_f32_e32 v146, 0.5, v146
	v_mul_f32_e32 v154, 0x38808081, v146
	v_med3_f32 v10, v10, s60, v200
	v_med3_f32 v152, v152, s60, v200
	v_mov_b32_e32 v146, v11
	v_max_f32_e32 v153, 0.5, v153
	v_cvt_pk_fp8_f32 v146, v10, v152
	v_mul_f32_e32 v153, 0x38808081, v153
	v_mul_f32_e32 v153, v44, v153
	v_mul_f32_e32 v10, v45, v154
	v_med3_f32 v152, v153, s60, v200
	v_med3_f32 v10, v10, s60, v200
	v_cvt_pk_fp8_f32 v146, v152, v10 op_sel:[0,0,1]
	v_cvt_f32_ubyte0_e32 v10, v147
	v_cvt_f32_ubyte1_e32 v152, v147
	v_max_f32_e32 v10, 0.5, v10
	v_max_f32_e32 v152, 0.5, v152
	v_cvt_f32_ubyte2_e32 v153, v147
	v_cvt_f32_ubyte3_e32 v147, v147
	v_mul_f32_e32 v10, 0x38808081, v10
	v_mul_f32_e32 v152, 0x38808081, v152
	v_mul_f32_e32 v10, v38, v10
	v_mul_f32_e32 v152, v39, v152
	v_max_f32_e32 v147, 0.5, v147
	v_mul_f32_e32 v154, 0x38808081, v147
	v_med3_f32 v10, v10, s60, v200
	v_med3_f32 v152, v152, s60, v200
	v_mov_b32_e32 v147, v11
	v_max_f32_e32 v153, 0.5, v153
	v_cvt_pk_fp8_f32 v147, v10, v152
	v_mul_f32_e32 v153, 0x38808081, v153
	v_mul_f32_e32 v153, v40, v153
	v_mul_f32_e32 v10, v41, v154
	v_med3_f32 v152, v153, s60, v200
	v_med3_f32 v10, v10, s60, v200
	v_cvt_pk_fp8_f32 v147, v152, v10 op_sel:[0,0,1]
	v_add_u32_e32 v152, s28, v194
	v_ashrrev_i32_e32 v153, 31, v152
	v_lshrrev_b64 v[154:155], 4, v[152:153]
	v_and_b32_e32 v155, 0x1ffff, v155
	v_and_b32_e32 v154, -16, v154
	v_lshl_add_u64 v[154:155], v[154:155], 0, s[26:27]
	v_lshlrev_b64 v[154:155], 15, v[154:155]
	v_lshlrev_b32_e32 v10, 7, v152
	v_and_b32_e32 v10, 0x7f80, v10
	v_lshl_add_u64 v[152:153], s[12:13], 0, v[154:155]
	v_lshl_add_u64 v[152:153], v[152:153], 0, v[10:11]
	v_lshl_add_u64 v[152:153], v[152:153], 0, v[178:179]
	global_store_dwordx4 v[152:153], v[144:147], off
	s_waitcnt vmcnt(0) lgkmcnt(0)
	v_cvt_f32_ubyte0_e32 v10, v148
	v_max_f32_e32 v10, 0.5, v10
	v_cvt_f32_ubyte1_e32 v144, v148
	v_max_f32_e32 v144, 0.5, v144
	v_mul_f32_e32 v10, 0x38808081, v10
	v_mul_f32_e32 v144, 0x38808081, v144
	v_mul_f32_e32 v10, v66, v10
	v_mul_f32_e32 v144, v67, v144
	v_cvt_f32_ubyte2_e32 v145, v148
	v_cvt_f32_ubyte3_e32 v146, v148
	v_med3_f32 v10, v10, s60, v200
	v_med3_f32 v147, v144, s60, v200
	v_mov_b32_e32 v144, v11
	v_max_f32_e32 v145, 0.5, v145
	v_max_f32_e32 v146, 0.5, v146
	v_cvt_pk_fp8_f32 v144, v10, v147
	v_mul_f32_e32 v145, 0x38808081, v145
	v_mul_f32_e32 v146, 0x38808081, v146
	v_mul_f32_e32 v145, v68, v145
	v_mul_f32_e32 v10, v69, v146
	v_med3_f32 v145, v145, s60, v200
	v_med3_f32 v10, v10, s60, v200
	v_cvt_pk_fp8_f32 v144, v145, v10 op_sel:[0,0,1]
	v_cvt_f32_ubyte0_e32 v10, v149
	v_cvt_f32_ubyte1_e32 v145, v149
	v_max_f32_e32 v10, 0.5, v10
	v_max_f32_e32 v145, 0.5, v145
	v_mul_f32_e32 v10, 0x38808081, v10
	v_mul_f32_e32 v145, 0x38808081, v145
	v_mul_f32_e32 v10, v62, v10
	v_mul_f32_e32 v145, v63, v145
	v_cvt_f32_ubyte2_e32 v146, v149
	v_cvt_f32_ubyte3_e32 v147, v149
	v_med3_f32 v10, v10, s60, v200
	v_med3_f32 v148, v145, s60, v200
	v_mov_b32_e32 v145, v11
	v_max_f32_e32 v146, 0.5, v146
	v_max_f32_e32 v147, 0.5, v147
	v_cvt_pk_fp8_f32 v145, v10, v148
	v_mul_f32_e32 v146, 0x38808081, v146
	v_mul_f32_e32 v147, 0x38808081, v147
	v_mul_f32_e32 v146, v64, v146
	v_mul_f32_e32 v10, v65, v147
	v_med3_f32 v146, v146, s60, v200
	v_med3_f32 v10, v10, s60, v200
	v_cvt_pk_fp8_f32 v145, v146, v10 op_sel:[0,0,1]
	v_cvt_f32_ubyte0_e32 v10, v150
	v_cvt_f32_ubyte1_e32 v146, v150
	v_max_f32_e32 v10, 0.5, v10
	v_max_f32_e32 v146, 0.5, v146
	v_mul_f32_e32 v10, 0x38808081, v10
	v_mul_f32_e32 v146, 0x38808081, v146
	v_mul_f32_e32 v10, v34, v10
	v_mul_f32_e32 v146, v35, v146
	v_cvt_f32_ubyte2_e32 v147, v150
	v_cvt_f32_ubyte3_e32 v148, v150
	v_med3_f32 v10, v10, s60, v200
	v_med3_f32 v149, v146, s60, v200
	v_mov_b32_e32 v146, v11
	v_max_f32_e32 v147, 0.5, v147
	v_max_f32_e32 v148, 0.5, v148
	v_cvt_pk_fp8_f32 v146, v10, v149
	v_mul_f32_e32 v147, 0x38808081, v147
	v_mul_f32_e32 v148, 0x38808081, v148
	v_mul_f32_e32 v147, v36, v147
	v_mul_f32_e32 v10, v37, v148
	v_med3_f32 v147, v147, s60, v200
	v_med3_f32 v10, v10, s60, v200
	v_cvt_pk_fp8_f32 v146, v147, v10 op_sel:[0,0,1]
	v_cvt_f32_ubyte0_e32 v10, v151
	v_cvt_f32_ubyte1_e32 v147, v151
	v_max_f32_e32 v10, 0.5, v10
	v_max_f32_e32 v147, 0.5, v147
	v_mul_f32_e32 v10, 0x38808081, v10
	v_mul_f32_e32 v147, 0x38808081, v147
	v_mul_f32_e32 v10, v30, v10
	v_mul_f32_e32 v147, v31, v147
	v_cvt_f32_ubyte2_e32 v148, v151
	v_cvt_f32_ubyte3_e32 v149, v151
	v_med3_f32 v10, v10, s60, v200
	v_med3_f32 v150, v147, s60, v200
	v_mov_b32_e32 v147, v11
	v_max_f32_e32 v148, 0.5, v148
	v_max_f32_e32 v149, 0.5, v149
	v_cvt_pk_fp8_f32 v147, v10, v150
	v_mul_f32_e32 v148, 0x38808081, v148
	v_mul_f32_e32 v149, 0x38808081, v149
	v_mul_f32_e32 v148, v32, v148
	v_mul_f32_e32 v10, v33, v149
	v_med3_f32 v148, v148, s60, v200
	v_med3_f32 v10, v10, s60, v200
	v_cvt_pk_fp8_f32 v147, v148, v10 op_sel:[0,0,1]
	v_add_u32_e32 v148, s28, v195
	v_ashrrev_i32_e32 v149, 31, v148
	v_lshrrev_b64 v[150:151], 4, v[148:149]
	v_and_b32_e32 v151, 0x1ffff, v151
	v_and_b32_e32 v150, -16, v150
	v_lshl_add_u64 v[150:151], v[150:151], 0, s[26:27]
	v_lshlrev_b64 v[150:151], 15, v[150:151]
	v_lshlrev_b32_e32 v10, 7, v148
	v_and_b32_e32 v10, 0x7f80, v10
	v_lshl_add_u64 v[148:149], s[12:13], 0, v[150:151]
; __device__ __forceinline__ f32x4 u8x4_f32(unsigned w) { return (f32x4){(float)(w & 0xffu), (float)((w >> 8) & 0xffu), (float)((w >> 16) & 0xffu), (float)(w >> 24)}; }
; __device__ __forceinline__ unsigned pk4_fp8(float a, float b, float c, float d) { int w = 0; w = __builtin_amdgcn_cvt_pk_fp8_f32(clamp8(a), clamp8(b), w, false); w = __builtin_amdgcn_cvt_pk_fp8_f32(clamp8(c), clamp8(d), w, true); return (unsigned)w; }
; __host__ __device__ __forceinline__ size_t tiled_off(size_t r, int kb, int ktiles) { return (((r >> 8) * ktiles + (kb >> 7)) << 15) + ((r & 255) << 7) + (kb & 127); }
;     __device__ __forceinline__ void operator()(f32x4 (&acc)[2][2][4][2], const GUnit& u, int wr, int wc, int fr, int fq) const {
;     ...
;             for (int m = 0; m < 4; ++m) qf[m] = __builtin_nontemporal_load((const u32x4*)(GZF + off0 + (size_t)(ai * 128 + m * 16) * D));
; #pragma unroll
;             for (int m = 0; m < 4; ++m) { u32x4 w;
; #pragma unroll
;                 for (int q = 0; q < 4; ++q) { const f32x4 f = u8x4_f32(qf[m][q]); const f32x4 a = acc[ai][q >> 1][m][q & 1]; f32x4 v;
; #pragma unroll
;                     for (int j = 0; j < 4; ++j) v[j] = a[j] * (fmaxf(f[j], 0.5f) * (W8_INV / 255.0f));
;                     w[q] = pk4_fp8(v[0], v[1], v[2], v[3]); }
;                 *(u32x4*)(M8 + tiled_off((size_t)(u.x0 * 256 + wr * 64 + fr + ai * 128 + m * 16), u.x1 * 256 + wc * 64 + 16 * fq, D / 128)) = w; }
;             asm volatile("" ::: "memory");
;         }
;     }
	v_lshl_add_u64 v[148:149], v[148:149], 0, v[10:11]
	v_lshl_add_u64 v[148:149], v[148:149], 0, v[178:179]
	global_store_dwordx4 v[148:149], v[144:147], off
	v_cvt_f32_ubyte0_e32 v10, v6
	v_max_f32_e32 v10, 0.5, v10
	v_cvt_f32_ubyte1_e32 v144, v6
	v_max_f32_e32 v144, 0.5, v144
	v_cvt_f32_ubyte2_e32 v145, v6
	v_cvt_f32_ubyte3_e32 v6, v6
	v_mul_f32_e32 v10, 0x38808081, v10
	v_mul_f32_e32 v144, 0x38808081, v144
	v_mul_f32_e32 v10, v58, v10
	v_mul_f32_e32 v144, v59, v144
	v_max_f32_e32 v6, 0.5, v6
	v_mul_f32_e32 v146, 0x38808081, v6
	v_med3_f32 v10, v10, s60, v200
	v_med3_f32 v144, v144, s60, v200
	v_mov_b32_e32 v6, v11
	v_max_f32_e32 v145, 0.5, v145
	v_cvt_pk_fp8_f32 v6, v10, v144
	v_mul_f32_e32 v145, 0x38808081, v145
	v_mul_f32_e32 v145, v60, v145
	v_mul_f32_e32 v10, v61, v146
	v_med3_f32 v144, v145, s60, v200
	v_med3_f32 v10, v10, s60, v200
	v_cvt_pk_fp8_f32 v6, v144, v10 op_sel:[0,0,1]
	v_cvt_f32_ubyte0_e32 v10, v7
	v_cvt_f32_ubyte1_e32 v144, v7
	v_max_f32_e32 v10, 0.5, v10
	v_max_f32_e32 v144, 0.5, v144
	v_cvt_f32_ubyte2_e32 v145, v7
	v_cvt_f32_ubyte3_e32 v7, v7
	v_mul_f32_e32 v10, 0x38808081, v10
	v_mul_f32_e32 v144, 0x38808081, v144
	v_mul_f32_e32 v10, v54, v10
	v_mul_f32_e32 v144, v55, v144
	v_max_f32_e32 v7, 0.5, v7
	v_mul_f32_e32 v146, 0x38808081, v7
	v_med3_f32 v10, v10, s60, v200
	v_med3_f32 v144, v144, s60, v200
	v_mov_b32_e32 v7, v11
	v_max_f32_e32 v145, 0.5, v145
	v_cvt_pk_fp8_f32 v7, v10, v144
	v_mul_f32_e32 v145, 0x38808081, v145
	v_mul_f32_e32 v145, v56, v145
	v_mul_f32_e32 v10, v57, v146
	v_med3_f32 v144, v145, s60, v200
	v_med3_f32 v10, v10, s60, v200
	v_cvt_pk_fp8_f32 v7, v144, v10 op_sel:[0,0,1]
	v_cvt_f32_ubyte0_e32 v10, v8
	v_cvt_f32_ubyte1_e32 v144, v8
	v_max_f32_e32 v10, 0.5, v10
	v_max_f32_e32 v144, 0.5, v144
	v_cvt_f32_ubyte2_e32 v145, v8
	v_cvt_f32_ubyte3_e32 v8, v8
	v_mul_f32_e32 v10, 0x38808081, v10
	v_mul_f32_e32 v144, 0x38808081, v144
	v_mul_f32_e32 v10, v26, v10
	v_mul_f32_e32 v144, v27, v144
	v_max_f32_e32 v8, 0.5, v8
	v_mul_f32_e32 v146, 0x38808081, v8
	v_med3_f32 v10, v10, s60, v200
	v_med3_f32 v144, v144, s60, v200
	v_mov_b32_e32 v8, v11
	v_max_f32_e32 v145, 0.5, v145
	v_cvt_pk_fp8_f32 v8, v10, v144
	v_mul_f32_e32 v145, 0x38808081, v145
	v_mul_f32_e32 v145, v28, v145
	v_mul_f32_e32 v10, v29, v146
	v_med3_f32 v144, v145, s60, v200
	v_med3_f32 v10, v10, s60, v200
	v_cvt_pk_fp8_f32 v8, v144, v10 op_sel:[0,0,1]
	v_cvt_f32_ubyte0_e32 v10, v9
	v_cvt_f32_ubyte1_e32 v144, v9
	v_max_f32_e32 v10, 0.5, v10
	v_max_f32_e32 v144, 0.5, v144
	v_cvt_f32_ubyte2_e32 v145, v9
	v_cvt_f32_ubyte3_e32 v9, v9
	v_mul_f32_e32 v10, 0x38808081, v10
	v_mul_f32_e32 v144, 0x38808081, v144
	v_mul_f32_e32 v10, v22, v10
	v_mul_f32_e32 v144, v23, v144
	v_max_f32_e32 v9, 0.5, v9
	v_mul_f32_e32 v146, 0x38808081, v9
	v_med3_f32 v10, v10, s60, v200
	v_med3_f32 v144, v144, s60, v200
	v_mov_b32_e32 v9, v11
	v_max_f32_e32 v145, 0.5, v145
	v_cvt_pk_fp8_f32 v9, v10, v144
	v_mul_f32_e32 v145, 0x38808081, v145
	v_mul_f32_e32 v145, v24, v145
	v_mul_f32_e32 v10, v25, v146
	v_med3_f32 v144, v145, s60, v200
	v_med3_f32 v10, v10, s60, v200
	v_cvt_pk_fp8_f32 v9, v144, v10 op_sel:[0,0,1]
	v_add_u32_e32 v144, s28, v196
	v_ashrrev_i32_e32 v145, 31, v144
	v_lshrrev_b64 v[146:147], 4, v[144:145]
	v_and_b32_e32 v147, 0x1ffff, v147
	v_and_b32_e32 v146, -16, v146
	v_lshl_add_u64 v[146:147], v[146:147], 0, s[26:27]
	v_lshlrev_b64 v[146:147], 15, v[146:147]
	v_lshlrev_b32_e32 v10, 7, v144
	v_and_b32_e32 v10, 0x7f80, v10
	v_lshl_add_u64 v[144:145], s[12:13], 0, v[146:147]
	v_lshl_add_u64 v[144:145], v[144:145], 0, v[10:11]
	v_lshl_add_u64 v[144:145], v[144:145], 0, v[178:179]
	global_store_dwordx4 v[144:145], v[6:9], off
	s_nop 1
	v_cvt_f32_ubyte0_e32 v6, v2
	v_cvt_f32_ubyte1_e32 v7, v2
	v_max_f32_e32 v6, 0.5, v6
	v_max_f32_e32 v7, 0.5, v7
	v_cvt_f32_ubyte2_e32 v8, v2
	v_cvt_f32_ubyte3_e32 v2, v2
	v_mul_f32_e32 v6, 0x38808081, v6
	v_mul_f32_e32 v7, 0x38808081, v7
	v_mul_f32_e32 v6, v50, v6
	v_mul_f32_e32 v7, v51, v7
	v_max_f32_e32 v2, 0.5, v2
	v_mul_f32_e32 v9, 0x38808081, v2
	v_med3_f32 v6, v6, s60, v200
	v_med3_f32 v7, v7, s60, v200
	v_mov_b32_e32 v2, v11
	v_max_f32_e32 v8, 0.5, v8
	v_cvt_pk_fp8_f32 v2, v6, v7
	v_mul_f32_e32 v8, 0x38808081, v8
	v_mul_f32_e32 v8, v52, v8
	v_mul_f32_e32 v6, v53, v9
	v_med3_f32 v7, v8, s60, v200
	v_med3_f32 v6, v6, s60, v200
	v_cvt_pk_fp8_f32 v2, v7, v6 op_sel:[0,0,1]
	v_cvt_f32_ubyte0_e32 v6, v3
	v_cvt_f32_ubyte1_e32 v7, v3
	v_max_f32_e32 v6, 0.5, v6
	v_max_f32_e32 v7, 0.5, v7
	v_cvt_f32_ubyte2_e32 v8, v3
	v_cvt_f32_ubyte3_e32 v3, v3
	v_mul_f32_e32 v6, 0x38808081, v6
	v_mul_f32_e32 v7, 0x38808081, v7
	v_mul_f32_e32 v6, v46, v6
	v_mul_f32_e32 v7, v47, v7
	v_max_f32_e32 v3, 0.5, v3
	v_mul_f32_e32 v9, 0x38808081, v3
	v_med3_f32 v6, v6, s60, v200
	v_med3_f32 v7, v7, s60, v200
	v_mov_b32_e32 v3, v11
	v_max_f32_e32 v8, 0.5, v8
	v_cvt_pk_fp8_f32 v3, v6, v7
	v_mul_f32_e32 v8, 0x38808081, v8
	v_mul_f32_e32 v8, v48, v8
	v_mul_f32_e32 v6, v49, v9
	v_med3_f32 v7, v8, s60, v200
	v_med3_f32 v6, v6, s60, v200
	v_cvt_pk_fp8_f32 v3, v7, v6 op_sel:[0,0,1]
	v_cvt_f32_ubyte0_e32 v6, v4
	v_cvt_f32_ubyte1_e32 v7, v4
	v_max_f32_e32 v6, 0.5, v6
	v_max_f32_e32 v7, 0.5, v7
	v_cvt_f32_ubyte2_e32 v8, v4
	v_cvt_f32_ubyte3_e32 v4, v4
	v_mul_f32_e32 v6, 0x38808081, v6
	v_mul_f32_e32 v7, 0x38808081, v7
	v_mul_f32_e32 v6, v18, v6
	v_mul_f32_e32 v7, v19, v7
	v_max_f32_e32 v4, 0.5, v4
	v_mul_f32_e32 v9, 0x38808081, v4
	v_med3_f32 v6, v6, s60, v200
	v_med3_f32 v7, v7, s60, v200
	v_mov_b32_e32 v4, v11
	v_max_f32_e32 v8, 0.5, v8
	v_cvt_pk_fp8_f32 v4, v6, v7
	v_mul_f32_e32 v8, 0x38808081, v8
	v_mul_f32_e32 v8, v20, v8
	v_mul_f32_e32 v6, v21, v9
	v_med3_f32 v7, v8, s60, v200
	v_med3_f32 v6, v6, s60, v200
	v_cvt_pk_fp8_f32 v4, v7, v6 op_sel:[0,0,1]
	v_cvt_f32_ubyte0_e32 v6, v5
	v_cvt_f32_ubyte1_e32 v7, v5
	v_max_f32_e32 v6, 0.5, v6
	v_max_f32_e32 v7, 0.5, v7
	v_cvt_f32_ubyte2_e32 v8, v5
	v_cvt_f32_ubyte3_e32 v5, v5
	v_mul_f32_e32 v6, 0x38808081, v6
	v_mul_f32_e32 v7, 0x38808081, v7
	v_mul_f32_e32 v6, v14, v6
	v_mul_f32_e32 v7, v15, v7
	v_max_f32_e32 v5, 0.5, v5
	v_mul_f32_e32 v9, 0x38808081, v5
	v_med3_f32 v6, v6, s60, v200
	v_med3_f32 v7, v7, s60, v200
	v_mov_b32_e32 v5, v11
	v_max_f32_e32 v8, 0.5, v8
	v_cvt_pk_fp8_f32 v5, v6, v7
	v_mul_f32_e32 v8, 0x38808081, v8
	v_mul_f32_e32 v8, v16, v8
	v_mul_f32_e32 v6, v17, v9
	v_med3_f32 v7, v8, s60, v200
	v_med3_f32 v6, v6, s60, v200
	v_cvt_pk_fp8_f32 v5, v7, v6 op_sel:[0,0,1]
	v_add_u32_e32 v6, s28, v197
	v_ashrrev_i32_e32 v7, 31, v6
	v_lshrrev_b64 v[8:9], 4, v[6:7]
	v_and_b32_e32 v9, 0x1ffff, v9
	v_and_b32_e32 v8, -16, v8
	v_lshl_add_u64 v[8:9], v[8:9], 0, s[26:27]
	v_lshlrev_b64 v[8:9], 15, v[8:9]
	v_lshlrev_b32_e32 v6, 7, v6
	v_and_b32_e32 v10, 0x7f80, v6
	v_lshl_add_u64 v[6:7], s[12:13], 0, v[8:9]
	v_lshl_add_u64 v[6:7], v[6:7], 0, v[10:11]
	v_lshl_add_u64 v[6:7], v[6:7], 0, v[178:179]
	global_store_dwordx4 v[6:7], v[2:5], off
	s_cbranch_execnz .LBB0_840

; __device__ __forceinline__ unsigned pk4_fp8(float a, float b, float c, float d) { int w = 0; w = __builtin_amdgcn_cvt_pk_fp8_f32(clamp8(a), clamp8(b), w, false); w = __builtin_amdgcn_cvt_pk_fp8_f32(clamp8(c), clamp8(d), w, true); return (unsigned)w; }
;     __device__ __forceinline__ void operator()(AccRef acc, const GUnit& u, int wr, int wc, int fr, int fq) const {
;         const int pm = u.x0, pn = u.x1; const float* gate = modv + (size_t)(pm >> 5) * 12288 + 2 * D;
;         const int col0 = pn * 256 + wc * 64 + 16 * fq;
;         f32x4 gv[4];
; #pragma unroll
;         for (int q = 0; q < 4; ++q) gv[q] = *(const f32x4*)(gate + col0 + 4 * q) * (W8_INV * MG8_SCALE);
; #pragma unroll
;         for (int ai = 0; ai < 2; ++ai)
; #pragma unroll
;             for (int m = 0; m < 4; ++m) { u32x4 w;
; #pragma unroll
;                 for (int q = 0; q < 4; ++q) { const f32x4 v = acc[ai][q >> 1][m][q & 1] * gv[q]; w[q] = pk4_fp8(v[0], v[1], v[2], v[3]); }
;                 *(u32x4*)(MG + (size_t)(pm * 256 + ai * 128 + wr * 64 + m * 16 + fr) * D + col0) = w; }
.LBB0_914:
	s_ashr_i32 s19, s26, 5
	s_mul_hi_i32 s21, s19, 0xc000
	s_mul_i32 s19, s19, 0xc000
	s_add_u32 s28, s36, s19
	v_lshl_or_b32 v2, s64, 8, v190
	s_addc_u32 s29, s37, s21
	v_ashrrev_i32_e32 v3, 31, v2
	v_lshl_add_u64 v[4:5], v[2:3], 2, s[28:29]
	v_add_co_u32_e32 v6, vcc, s62, v4
	s_nop 15
	s_nop 7
	s_nop 1
	v_addc_co_u32_e32 v7, vcc, 0, v5, vcc
	global_load_dwordx4 v[6:9], v[6:7], off
	v_lshl_add_u64 v[4:5], v[4:5], 0, s[14:15]
	global_load_dwordx4 v[10:13], v[4:5], off offset:16
	global_load_dwordx4 v[22:25], v[4:5], off offset:32
	global_load_dwordx4 v[26:29], v[4:5], off offset:48
	v_lshl_add_u32 v4, s26, 8, v188
	v_ashrrev_i32_e32 v5, 31, v4
	v_mov_b32_e32 v30, 0
	v_lshlrev_b64 v[14:15], 11, v[4:5]
	v_lshl_add_u64 v[14:15], s[10:11], 0, v[14:15]
	v_lshl_add_u64 v[200:201], v[14:15], 0, v[2:3]
	v_mov_b32_e32 v199, 0
	v_mov_b32_e32 v196, 0
	v_mov_b32_e32 v197, 0
	v_mov_b32_e32 v198, 0
	v_mov_b32_e32 v31, 0
	v_mov_b32_e32 v32, 0
	v_mov_b32_e32 v33, 0
	s_andn2_b64 vcc, exec, s[0:1]
	s_mov_b64 s[0:1], -1
	s_waitcnt vmcnt(0) lgkmcnt(0)
	v_pk_mul_f32 v[16:17], v[10:11], s[16:17] op_sel_hi:[1,0]
	v_pk_mul_f32 v[20:21], v[6:7], s[16:17] op_sel_hi:[1,0]
	v_pk_mul_f32 v[10:11], v[24:25], s[16:17] op_sel_hi:[1,0]
	v_pk_mul_f32 v[24:25], v[158:159], v[20:21]
	v_pk_mul_f32 v[18:19], v[8:9], s[16:17] op_sel_hi:[1,0]
	v_med3_f32 v5, v24, s63, v195
	v_med3_f32 v24, v25, s63, v195
	v_cvt_pk_fp8_f32 v30, v5, v24
	v_pk_mul_f32 v[14:15], v[12:13], s[16:17] op_sel_hi:[1,0]
	v_pk_mul_f32 v[12:13], v[22:23], s[16:17] op_sel_hi:[1,0]
	v_pk_mul_f32 v[22:23], v[160:161], v[18:19]
	v_pk_mul_f32 v[8:9], v[26:27], s[16:17] op_sel_hi:[1,0]
	v_med3_f32 v22, v22, s63, v195
	v_med3_f32 v23, v23, s63, v195
	v_cvt_pk_fp8_f32 v30, v22, v23 op_sel:[0,0,1]
	v_pk_mul_f32 v[22:23], v[126:127], v[8:9]
	v_pk_mul_f32 v[6:7], v[28:29], s[16:17] op_sel_hi:[1,0]
	v_pk_mul_f32 v[28:29], v[154:155], v[16:17]
	v_pk_mul_f32 v[144:145], v[144:145], v[10:11]
	v_pk_mul_f32 v[142:143], v[142:143], v[12:13]
	v_pk_mul_f32 v[150:151], v[150:151], v[20:21]
	v_pk_mul_f32 v[146:147], v[146:147], v[16:17]
	v_pk_mul_f32 v[134:135], v[134:135], v[12:13]
	v_med3_f32 v5, v22, s63, v195
	v_med3_f32 v22, v23, s63, v195
	v_med3_f32 v25, v28, s63, v195
	v_med3_f32 v28, v29, s63, v195
	v_med3_f32 v29, v142, s63, v195
	v_med3_f32 v142, v143, s63, v195
	v_med3_f32 v143, v144, s63, v195
	v_med3_f32 v144, v145, s63, v195
	v_med3_f32 v145, v150, s63, v195
	v_med3_f32 v150, v151, s63, v195
	v_med3_f32 v146, v146, s63, v195
	v_med3_f32 v147, v147, s63, v195
	v_med3_f32 v134, v134, s63, v195
	v_med3_f32 v135, v135, s63, v195
	v_cvt_pk_fp8_f32 v199, v5, v22
	v_cvt_pk_fp8_f32 v196, v145, v150
	v_cvt_pk_fp8_f32 v197, v146, v147
	v_cvt_pk_fp8_f32 v198, v134, v135
	v_pk_mul_f32 v[22:23], v[128:129], v[6:7]
	v_pk_mul_f32 v[152:153], v[152:153], v[18:19]
	v_pk_mul_f32 v[148:149], v[148:149], v[14:15]
	v_pk_mul_f32 v[136:137], v[136:137], v[10:11]
	v_med3_f32 v5, v22, s63, v195
	v_med3_f32 v22, v23, s63, v195
	v_med3_f32 v151, v152, s63, v195
	v_med3_f32 v152, v153, s63, v195
	v_med3_f32 v148, v148, s63, v195
	v_med3_f32 v149, v149, s63, v195
	v_med3_f32 v136, v136, s63, v195
	v_med3_f32 v137, v137, s63, v195
	v_cvt_pk_fp8_f32 v199, v5, v22 op_sel:[0,0,1]
	v_or_b32_e32 v22, 16, v4
	v_cvt_pk_fp8_f32 v196, v151, v152 op_sel:[0,0,1]
	v_cvt_pk_fp8_f32 v197, v148, v149 op_sel:[0,0,1]
	v_cvt_pk_fp8_f32 v198, v136, v137 op_sel:[0,0,1]
	v_ashrrev_i32_e32 v23, 31, v22
	v_lshlrev_b64 v[22:23], 11, v[22:23]
	v_lshl_add_u64 v[22:23], s[10:11], 0, v[22:23]
	v_lshl_add_u64 v[22:23], v[22:23], 0, v[2:3]
	global_store_dwordx4 v[22:23], v[196:199], off
	v_pk_mul_f32 v[22:23], v[130:131], v[20:21]
	v_cvt_pk_fp8_f32 v31, v25, v28
	v_med3_f32 v5, v22, s63, v195
	v_med3_f32 v23, v23, s63, v195
	v_mov_b32_e32 v22, 0
	v_cvt_pk_fp8_f32 v22, v5, v23
	v_pk_mul_f32 v[24:25], v[132:133], v[18:19]
	v_pk_mul_f32 v[26:27], v[156:157], v[14:15]
	v_med3_f32 v5, v24, s63, v195
	v_med3_f32 v23, v25, s63, v195
	v_pk_mul_f32 v[24:25], v[122:123], v[16:17]
	v_cvt_pk_fp8_f32 v22, v5, v23 op_sel:[0,0,1]
	v_med3_f32 v5, v24, s63, v195
	v_med3_f32 v24, v25, s63, v195
	v_mov_b32_e32 v23, 0
	v_cvt_pk_fp8_f32 v23, v5, v24
	v_pk_mul_f32 v[24:25], v[124:125], v[14:15]
	v_med3_f32 v26, v26, s63, v195
	v_med3_f32 v5, v24, s63, v195
	v_med3_f32 v24, v25, s63, v195
	v_cvt_pk_fp8_f32 v23, v5, v24 op_sel:[0,0,1]
	v_pk_mul_f32 v[24:25], v[118:119], v[12:13]
	v_med3_f32 v27, v27, s63, v195
	v_med3_f32 v5, v24, s63, v195
	v_med3_f32 v25, v25, s63, v195
	v_mov_b32_e32 v24, 0
	v_cvt_pk_fp8_f32 v24, v5, v25
	v_cvt_pk_fp8_f32 v31, v26, v27 op_sel:[0,0,1]
	v_pk_mul_f32 v[26:27], v[120:121], v[10:11]
	v_cvt_pk_fp8_f32 v32, v29, v142
	v_med3_f32 v5, v26, s63, v195
	v_med3_f32 v25, v27, s63, v195
	v_pk_mul_f32 v[26:27], v[110:111], v[8:9]
	v_cvt_pk_fp8_f32 v24, v5, v25 op_sel:[0,0,1]
	v_med3_f32 v5, v26, s63, v195
	v_med3_f32 v26, v27, s63, v195
	v_mov_b32_e32 v25, 0
	v_cvt_pk_fp8_f32 v25, v5, v26
	v_pk_mul_f32 v[26:27], v[112:113], v[6:7]
	v_pk_mul_f32 v[28:29], v[88:89], v[10:11]
	v_med3_f32 v5, v26, s63, v195
	v_med3_f32 v26, v27, s63, v195
	v_cvt_pk_fp8_f32 v25, v5, v26 op_sel:[0,0,1]
	v_or_b32_e32 v26, 32, v4
	v_ashrrev_i32_e32 v27, 31, v26
	v_lshlrev_b64 v[26:27], 11, v[26:27]
	v_lshl_add_u64 v[26:27], s[10:11], 0, v[26:27]
	v_lshl_add_u64 v[26:27], v[26:27], 0, v[2:3]
	global_store_dwordx4 v[26:27], v[22:25], off
	v_pk_mul_f32 v[26:27], v[104:105], v[10:11]
	v_pk_mul_f32 v[138:139], v[138:139], v[8:9]
	v_pk_mul_f32 v[22:23], v[114:115], v[20:21]
	v_pk_mul_f32 v[24:25], v[116:117], v[18:19]
	v_med3_f32 v5, v22, s63, v195
	v_med3_f32 v23, v23, s63, v195
	v_mov_b32_e32 v22, 0
; __device__ __forceinline__ unsigned pk4_fp8(float a, float b, float c, float d) { int w = 0; w = __builtin_amdgcn_cvt_pk_fp8_f32(clamp8(a), clamp8(b), w, false); w = __builtin_amdgcn_cvt_pk_fp8_f32(clamp8(c), clamp8(d), w, true); return (unsigned)w; }
;     __device__ __forceinline__ void operator()(AccRef acc, const GUnit& u, int wr, int wc, int fr, int fq) const {
;     ...
;         for (int ai = 0; ai < 2; ++ai)
; #pragma unroll
;             for (int m = 0; m < 4; ++m) { u32x4 w;
; #pragma unroll
;                 for (int q = 0; q < 4; ++q) { const f32x4 v = acc[ai][q >> 1][m][q & 1] * gv[q]; w[q] = pk4_fp8(v[0], v[1], v[2], v[3]); }
;                 *(u32x4*)(MG + (size_t)(pm * 256 + ai * 128 + wr * 64 + m * 16 + fr) * D + col0) = w; }
	v_cvt_pk_fp8_f32 v22, v5, v23
	v_med3_f32 v5, v24, s63, v195
	v_med3_f32 v23, v25, s63, v195
	v_pk_mul_f32 v[24:25], v[106:107], v[16:17]
	v_cvt_pk_fp8_f32 v22, v5, v23 op_sel:[0,0,1]
	v_med3_f32 v5, v24, s63, v195
	v_med3_f32 v24, v25, s63, v195
	v_mov_b32_e32 v23, 0
	v_cvt_pk_fp8_f32 v23, v5, v24
	v_pk_mul_f32 v[24:25], v[108:109], v[14:15]
	v_med3_f32 v138, v138, s63, v195
	v_med3_f32 v5, v24, s63, v195
	v_med3_f32 v24, v25, s63, v195
	v_cvt_pk_fp8_f32 v23, v5, v24 op_sel:[0,0,1]
	v_pk_mul_f32 v[24:25], v[102:103], v[12:13]
	v_med3_f32 v139, v139, s63, v195
	v_med3_f32 v5, v24, s63, v195
	v_med3_f32 v25, v25, s63, v195
	v_mov_b32_e32 v24, 0
	v_cvt_pk_fp8_f32 v24, v5, v25
	v_med3_f32 v5, v26, s63, v195
	v_med3_f32 v25, v27, s63, v195
	v_pk_mul_f32 v[26:27], v[98:99], v[8:9]
	v_cvt_pk_fp8_f32 v24, v5, v25 op_sel:[0,0,1]
	v_med3_f32 v5, v26, s63, v195
	v_med3_f32 v26, v27, s63, v195
	v_mov_b32_e32 v25, 0
	v_cvt_pk_fp8_f32 v25, v5, v26
	v_pk_mul_f32 v[26:27], v[100:101], v[6:7]
	v_cvt_pk_fp8_f32 v33, v138, v139
	v_med3_f32 v5, v26, s63, v195
	v_med3_f32 v26, v27, s63, v195
	v_cvt_pk_fp8_f32 v25, v5, v26 op_sel:[0,0,1]
	v_or_b32_e32 v26, 48, v4
	v_ashrrev_i32_e32 v27, 31, v26
	v_lshlrev_b64 v[26:27], 11, v[26:27]
	v_lshl_add_u64 v[26:27], s[10:11], 0, v[26:27]
	v_lshl_add_u64 v[26:27], v[26:27], 0, v[2:3]
	global_store_dwordx4 v[26:27], v[22:25], off
	v_add_u32_e32 v26, 0x80, v4
	v_pk_mul_f32 v[140:141], v[140:141], v[6:7]
	v_pk_mul_f32 v[22:23], v[94:95], v[20:21]
	v_pk_mul_f32 v[24:25], v[96:97], v[18:19]
	v_med3_f32 v5, v22, s63, v195
	v_med3_f32 v23, v23, s63, v195
	v_mov_b32_e32 v22, 0
	v_cvt_pk_fp8_f32 v22, v5, v23
	v_med3_f32 v5, v24, s63, v195
	v_med3_f32 v23, v25, s63, v195
	v_pk_mul_f32 v[24:25], v[90:91], v[16:17]
	v_cvt_pk_fp8_f32 v22, v5, v23 op_sel:[0,0,1]
	v_med3_f32 v5, v24, s63, v195
	v_med3_f32 v24, v25, s63, v195
	v_mov_b32_e32 v23, 0
	v_cvt_pk_fp8_f32 v23, v5, v24
	v_pk_mul_f32 v[24:25], v[92:93], v[14:15]
	v_med3_f32 v140, v140, s63, v195
	v_med3_f32 v5, v24, s63, v195
	v_med3_f32 v24, v25, s63, v195
	v_cvt_pk_fp8_f32 v23, v5, v24 op_sel:[0,0,1]
	v_pk_mul_f32 v[24:25], v[86:87], v[12:13]
	v_med3_f32 v141, v141, s63, v195
	v_med3_f32 v5, v24, s63, v195
	v_med3_f32 v25, v25, s63, v195
	v_mov_b32_e32 v24, 0
	v_cvt_pk_fp8_f32 v24, v5, v25
	v_med3_f32 v5, v28, s63, v195
	v_med3_f32 v25, v29, s63, v195
	v_pk_mul_f32 v[28:29], v[78:79], v[8:9]
	v_cvt_pk_fp8_f32 v24, v5, v25 op_sel:[0,0,1]
	v_med3_f32 v5, v28, s63, v195
	v_med3_f32 v27, v29, s63, v195
	v_mov_b32_e32 v25, 0
	v_cvt_pk_fp8_f32 v25, v5, v27
	v_pk_mul_f32 v[28:29], v[80:81], v[6:7]
	v_cvt_pk_fp8_f32 v32, v143, v144 op_sel:[0,0,1]
	v_med3_f32 v5, v28, s63, v195
	v_med3_f32 v27, v29, s63, v195
	v_cvt_pk_fp8_f32 v25, v5, v27 op_sel:[0,0,1]
	v_ashrrev_i32_e32 v27, 31, v26
	v_lshlrev_b64 v[26:27], 11, v[26:27]
	v_lshl_add_u64 v[26:27], s[10:11], 0, v[26:27]
	v_lshl_add_u64 v[26:27], v[26:27], 0, v[2:3]
	global_store_dwordx4 v[26:27], v[22:25], off
	v_pk_mul_f32 v[26:27], v[72:73], v[10:11]
	v_cvt_pk_fp8_f32 v33, v140, v141 op_sel:[0,0,1]
	v_pk_mul_f32 v[22:23], v[82:83], v[20:21]
	v_pk_mul_f32 v[24:25], v[84:85], v[18:19]
	v_med3_f32 v5, v22, s63, v195
	v_med3_f32 v23, v23, s63, v195
	v_mov_b32_e32 v22, 0
	v_cvt_pk_fp8_f32 v22, v5, v23
	v_med3_f32 v5, v24, s63, v195
	v_med3_f32 v23, v25, s63, v195
	v_pk_mul_f32 v[24:25], v[74:75], v[16:17]
	v_cvt_pk_fp8_f32 v22, v5, v23 op_sel:[0,0,1]
	v_med3_f32 v5, v24, s63, v195
	v_med3_f32 v24, v25, s63, v195
	v_mov_b32_e32 v23, 0
	v_cvt_pk_fp8_f32 v23, v5, v24
	v_pk_mul_f32 v[24:25], v[76:77], v[14:15]
	global_store_dwordx4 v[200:201], v[30:33], off
	v_med3_f32 v5, v24, s63, v195
	v_med3_f32 v24, v25, s63, v195
	v_cvt_pk_fp8_f32 v23, v5, v24 op_sel:[0,0,1]
	v_pk_mul_f32 v[24:25], v[70:71], v[12:13]
	s_nop 0
; __device__ __forceinline__ unsigned pk4_fp8(float a, float b, float c, float d) { int w = 0; w = __builtin_amdgcn_cvt_pk_fp8_f32(clamp8(a), clamp8(b), w, false); w = __builtin_amdgcn_cvt_pk_fp8_f32(clamp8(c), clamp8(d), w, true); return (unsigned)w; }
;     __device__ __forceinline__ void operator()(AccRef acc, const GUnit& u, int wr, int wc, int fr, int fq) const {
;     ...
;         for (int ai = 0; ai < 2; ++ai)
; #pragma unroll
;             for (int m = 0; m < 4; ++m) { u32x4 w;
; #pragma unroll
;                 for (int q = 0; q < 4; ++q) { const f32x4 v = acc[ai][q >> 1][m][q & 1] * gv[q]; w[q] = pk4_fp8(v[0], v[1], v[2], v[3]); }
;                 *(u32x4*)(MG + (size_t)(pm * 256 + ai * 128 + wr * 64 + m * 16 + fr) * D + col0) = w; }
	v_med3_f32 v5, v24, s63, v195
	v_med3_f32 v25, v25, s63, v195
	v_mov_b32_e32 v24, 0
	v_cvt_pk_fp8_f32 v24, v5, v25
	v_med3_f32 v5, v26, s63, v195
	v_med3_f32 v25, v27, s63, v195
	v_pk_mul_f32 v[26:27], v[62:63], v[8:9]
	v_cvt_pk_fp8_f32 v24, v5, v25 op_sel:[0,0,1]
	v_med3_f32 v5, v26, s63, v195
	v_med3_f32 v26, v27, s63, v195
	v_mov_b32_e32 v25, 0
	v_cvt_pk_fp8_f32 v25, v5, v26
	v_pk_mul_f32 v[26:27], v[64:65], v[6:7]
	s_nop 0
	v_med3_f32 v5, v26, s63, v195
	v_med3_f32 v26, v27, s63, v195
	v_cvt_pk_fp8_f32 v25, v5, v26 op_sel:[0,0,1]
	v_add_u32_e32 v26, 0x90, v4
	v_ashrrev_i32_e32 v27, 31, v26
	v_lshlrev_b64 v[26:27], 11, v[26:27]
	v_lshl_add_u64 v[26:27], s[10:11], 0, v[26:27]
	v_lshl_add_u64 v[26:27], v[26:27], 0, v[2:3]
	global_store_dwordx4 v[26:27], v[22:25], off
	v_pk_mul_f32 v[26:27], v[56:57], v[10:11]
	v_pk_mul_f32 v[10:11], v[40:41], v[10:11]
	v_pk_mul_f32 v[22:23], v[66:67], v[20:21]
	v_pk_mul_f32 v[24:25], v[68:69], v[18:19]
	v_med3_f32 v5, v22, s63, v195
	v_med3_f32 v23, v23, s63, v195
	v_mov_b32_e32 v22, 0
	v_cvt_pk_fp8_f32 v22, v5, v23
	v_med3_f32 v5, v24, s63, v195
	v_med3_f32 v23, v25, s63, v195
	v_pk_mul_f32 v[24:25], v[58:59], v[16:17]
	v_cvt_pk_fp8_f32 v22, v5, v23 op_sel:[0,0,1]
	v_med3_f32 v5, v24, s63, v195
	v_med3_f32 v24, v25, s63, v195
	v_mov_b32_e32 v23, 0
	v_cvt_pk_fp8_f32 v23, v5, v24
	v_pk_mul_f32 v[24:25], v[60:61], v[14:15]
	v_pk_mul_f32 v[20:21], v[50:51], v[20:21]
	v_med3_f32 v5, v24, s63, v195
	v_med3_f32 v24, v25, s63, v195
	v_cvt_pk_fp8_f32 v23, v5, v24 op_sel:[0,0,1]
	v_pk_mul_f32 v[24:25], v[54:55], v[12:13]
	v_med3_f32 v21, v21, s63, v195
	v_med3_f32 v5, v24, s63, v195
	v_med3_f32 v25, v25, s63, v195
	v_mov_b32_e32 v24, 0
	v_cvt_pk_fp8_f32 v24, v5, v25
	v_med3_f32 v5, v26, s63, v195
	v_med3_f32 v25, v27, s63, v195
	v_pk_mul_f32 v[26:27], v[46:47], v[8:9]
	v_cvt_pk_fp8_f32 v24, v5, v25 op_sel:[0,0,1]
	v_med3_f32 v5, v26, s63, v195
	v_med3_f32 v26, v27, s63, v195
	v_mov_b32_e32 v25, 0
	v_cvt_pk_fp8_f32 v25, v5, v26
	v_pk_mul_f32 v[26:27], v[48:49], v[6:7]
	v_pk_mul_f32 v[18:19], v[52:53], v[18:19]
	v_med3_f32 v5, v26, s63, v195
	v_med3_f32 v26, v27, s63, v195
	v_cvt_pk_fp8_f32 v25, v5, v26 op_sel:[0,0,1]
	v_med3_f32 v5, v20, s63, v195
	v_mov_b32_e32 v20, 0
	v_cvt_pk_fp8_f32 v20, v5, v21
	v_med3_f32 v5, v18, s63, v195
	v_med3_f32 v18, v19, s63, v195
	v_pk_mul_f32 v[16:17], v[42:43], v[16:17]
	v_add_u32_e32 v26, 0xa0, v4
	v_cvt_pk_fp8_f32 v20, v5, v18 op_sel:[0,0,1]
	v_med3_f32 v5, v16, s63, v195
	v_med3_f32 v16, v17, s63, v195
	v_mov_b32_e32 v21, 0
	v_ashrrev_i32_e32 v27, 31, v26
	v_cvt_pk_fp8_f32 v21, v5, v16
	v_lshlrev_b64 v[26:27], 11, v[26:27]
	v_lshl_add_u64 v[26:27], s[10:11], 0, v[26:27]
	v_pk_mul_f32 v[14:15], v[44:45], v[14:15]
	v_lshl_add_u64 v[26:27], v[26:27], 0, v[2:3]
	v_med3_f32 v5, v14, s63, v195
	v_med3_f32 v14, v15, s63, v195
	v_pk_mul_f32 v[12:13], v[38:39], v[12:13]
	global_store_dwordx4 v[26:27], v[22:25], off
	v_cvt_pk_fp8_f32 v21, v5, v14 op_sel:[0,0,1]
	v_med3_f32 v5, v12, s63, v195
	v_med3_f32 v12, v13, s63, v195
	v_mov_b32_e32 v22, 0
	v_cvt_pk_fp8_f32 v22, v5, v12
	v_med3_f32 v5, v10, s63, v195
	v_med3_f32 v10, v11, s63, v195
	v_pk_mul_f32 v[8:9], v[34:35], v[8:9]
	v_cvt_pk_fp8_f32 v22, v5, v10 op_sel:[0,0,1]
	v_med3_f32 v5, v8, s63, v195
	v_med3_f32 v8, v9, s63, v195
	v_mov_b32_e32 v23, 0
	v_cvt_pk_fp8_f32 v23, v5, v8
	v_pk_mul_f32 v[6:7], v[36:37], v[6:7]
	v_add_u32_e32 v4, 0xb0, v4
	v_med3_f32 v5, v6, s63, v195
	v_med3_f32 v6, v7, s63, v195
	v_cvt_pk_fp8_f32 v23, v5, v6 op_sel:[0,0,1]
	v_ashrrev_i32_e32 v5, 31, v4
	v_lshlrev_b64 v[4:5], 11, v[4:5]
	v_lshl_add_u64 v[4:5], s[10:11], 0, v[4:5]
	v_lshl_add_u64 v[2:3], v[4:5], 0, v[2:3]
	global_store_dwordx4 v[2:3], v[20:23], off
	s_cbranch_vccnz .LBB0_903
	s_andn2_b64 vcc, exec, s[8:9]
	s_cbranch_vccnz .LBB0_902
	s_branch .LBB0_902

; __device__ __forceinline__ float fsigmoid(float x) { return __builtin_amdgcn_rcpf(1.0f + __builtin_amdgcn_exp2f(-1.44269504f * x)); }
; __device__ __forceinline__ unsigned pk4_fp8(float a, float b, float c, float d) { int w = 0; w = __builtin_amdgcn_cvt_pk_fp8_f32(clamp8(a), clamp8(b), w, false); w = __builtin_amdgcn_cvt_pk_fp8_f32(clamp8(c), clamp8(d), w, true); return (unsigned)w; }
;     __device__ __forceinline__ void operator()(AccRef acc, const GUnit& u, int wr, int wc, int fr, int fq) const {
;         const int e = u.x0, rt = u.x1, ct = u.x2, cnt = u.x3; const int p0 = rt * 256 + wr * 64 + fr;
;         const int odd = fq & 1;
;         unsigned char* blk = HID + ((size_t)((__builtin_amdgcn_readfirstlane(pre[e]) + rt) * (DE / 128) + ct) << 15) + (wr * 64 + fr) * 128 + wc * 32 + 16 * (fq >> 1);
; #pragma unroll
;         for (int ai = 0; ai < 2; ++ai)
; #pragma unroll
;             for (int mp = 0; mp < 4; mp += 2) {
;                 f32x4 v0, v1, w0, w1;
; #pragma unroll
;                 for (int j = 0; j < 4; ++j) { const float a0 = acc[ai][0][mp][0][j] * W8_INV, a1 = acc[ai][0][mp][1][j] * W8_INV; v0[j] = a0 * fsigmoid(a0) * (acc[ai][1][mp][0][j] * W8_INV); v1[j] = a1 * fsigmoid(a1) * (acc[ai][1][mp][1][j] * W8_INV); }
; #pragma unroll
;                 for (int j = 0; j < 4; ++j) { const float a0 = acc[ai][0][mp + 1][0][j] * W8_INV, a1 = acc[ai][0][mp + 1][1][j] * W8_INV; w0[j] = a0 * fsigmoid(a0) * (acc[ai][1][mp + 1][0][j] * W8_INV); w1[j] = a1 * fsigmoid(a1) * (acc[ai][1][mp + 1][1][j] * W8_INV); }
;                 const unsigned lo0 = pk4_fp8(v0[0], v0[1], v0[2], v0[3]), hi0 = pk4_fp8(v1[0], v1[1], v1[2], v1[3]), lo1 = pk4_fp8(w0[0], w0[1], w0[2], w0[3]), hi1 = pk4_fp8(w1[0], w1[1], w1[2], w1[3]);
;                 const auto sl = __builtin_amdgcn_permlane16_swap(lo0, lo1, false, false), sh = __builtin_amdgcn_permlane16_swap(hi0, hi1, false, false);
;                 const int p = p0 + ai * 128 + (mp + odd) * 16;
;                 if (p < cnt) *(u32x4*)(blk + (ai * 128 + (mp + odd) * 16) * 128) = (u32x4){sl[0], sh[0], sl[1], sh[1]}; }
.LBB0_1064:
	s_lshl_b32 s21, s0, 2
	s_add_i32 s21, s21, 0
	s_add_i32 s21, s21, 0x24100
	v_mov_b32_e32 v2, s21
	s_nop 15
	s_nop 7
	ds_read_b32 v2, v2
	v_mul_f32_e32 v4, 0x3c800000, v138
	v_mul_f32_e32 v5, 0xbfb8aa3b, v4
	v_exp_f32_e32 v5, v5
	v_mul_f32_e32 v9, 0x3c800000, v139
	s_waitcnt lgkmcnt(0)
	v_readfirstlane_b32 s21, v2
	v_mul_f32_e32 v2, 0x3c800000, v142
	v_mul_f32_e32 v3, 0xbfb8aa3b, v2
	v_exp_f32_e32 v3, v3
	v_add_f32_e32 v5, 1.0, v5
	v_rcp_f32_e32 v5, v5
	v_mul_f32_e32 v11, 0xbfb8aa3b, v9
	v_add_f32_e32 v3, 1.0, v3
	v_rcp_f32_e32 v3, v3
	v_exp_f32_e32 v11, v11
	v_mul_f32_e32 v12, 0x3c800000, v140
	v_mul_f32_e32 v13, 0xbfb8aa3b, v12
	v_mul_f32_e32 v2, v2, v3
	v_mul_f32_e32 v3, 0x3c800000, v110
	v_mul_f32_e32 v2, v3, v2
	v_mul_f32_e32 v3, v4, v5
	v_mul_f32_e32 v5, 0x3c800000, v143
	v_mul_f32_e32 v8, 0xbfb8aa3b, v5
	v_exp_f32_e32 v8, v8
	v_mul_f32_e32 v4, 0x3c800000, v106
	v_mul_f32_e32 v3, v4, v3
	v_add_f32_e32 v4, 1.0, v11
	v_add_f32_e32 v8, 1.0, v8
	v_rcp_f32_e32 v8, v8
	v_rcp_f32_e32 v4, v4
	v_exp_f32_e32 v13, v13
	v_mul_f32_e32 v14, 0x3c800000, v141
	v_mul_f32_e32 v5, v5, v8
	v_mul_f32_e32 v8, 0x3c800000, v111
	v_mul_f32_e32 v5, v8, v5
	v_mul_f32_e32 v4, v9, v4
	v_mul_f32_e32 v8, 0x3c800000, v107
	v_mul_f32_e32 v9, 0x3c800000, v144
	v_mul_f32_e32 v11, 0xbfb8aa3b, v9
	v_mul_f32_e32 v4, v8, v4
	v_add_f32_e32 v8, 1.0, v13
	v_exp_f32_e32 v11, v11
	v_rcp_f32_e32 v8, v8
	v_mul_f32_e32 v15, 0xbfb8aa3b, v14
	v_exp_f32_e32 v15, v15
	v_add_f32_e32 v11, 1.0, v11
	v_mul_f32_e32 v8, v12, v8
	v_mul_f32_e32 v12, 0x3c800000, v145
	v_rcp_f32_e32 v11, v11
	v_mul_f32_e32 v13, 0xbfb8aa3b, v12
	v_exp_f32_e32 v13, v13
	v_mul_f32_e32 v16, 0x3c800000, v130
	v_mul_f32_e32 v9, v9, v11
	v_mul_f32_e32 v11, 0x3c800000, v112
	v_mul_f32_e32 v9, v11, v9
	v_mul_f32_e32 v11, 0x3c800000, v108
	v_add_f32_e32 v13, 1.0, v13
	v_rcp_f32_e32 v13, v13
	v_mul_f32_e32 v8, v11, v8
	v_add_f32_e32 v11, 1.0, v15
	v_rcp_f32_e32 v11, v11
	v_mul_f32_e32 v17, 0xbfb8aa3b, v16
	v_exp_f32_e32 v17, v17
	v_mul_f32_e32 v12, v12, v13
	v_mul_f32_e32 v13, 0x3c800000, v113
	v_mul_f32_e32 v12, v13, v12
	v_mul_f32_e32 v11, v14, v11
	v_mul_f32_e32 v13, 0x3c800000, v109
	v_mul_f32_e32 v14, 0x3c800000, v134
	v_mul_f32_e32 v15, 0xbfb8aa3b, v14
	v_mul_f32_e32 v11, v13, v11
	v_add_f32_e32 v13, 1.0, v17
	v_exp_f32_e32 v15, v15
	v_rcp_f32_e32 v13, v13
	v_mul_f32_e32 v18, 0x3c800000, v131
	v_mul_f32_e32 v19, 0xbfb8aa3b, v18
	v_add_f32_e32 v15, 1.0, v15
	v_mul_f32_e32 v13, v16, v13
	v_mul_f32_e32 v16, 0x3c800000, v135
	v_rcp_f32_e32 v15, v15
	v_mul_f32_e32 v17, 0xbfb8aa3b, v16
	v_exp_f32_e32 v17, v17
	v_exp_f32_e32 v19, v19
	v_mul_f32_e32 v14, v14, v15
	v_mul_f32_e32 v15, 0x3c800000, v102
	v_mul_f32_e32 v14, v15, v14
	v_mul_f32_e32 v15, 0x3c800000, v98
	v_add_f32_e32 v17, 1.0, v17
	v_rcp_f32_e32 v17, v17
	v_mul_f32_e32 v13, v15, v13
	v_add_f32_e32 v15, 1.0, v19
	v_mul_f32_e32 v20, 0x3c800000, v132
	v_rcp_f32_e32 v15, v15
	v_mul_f32_e32 v21, 0xbfb8aa3b, v20
	v_exp_f32_e32 v21, v21
	v_mul_f32_e32 v16, v16, v17
	v_mul_f32_e32 v17, 0x3c800000, v103
	v_mul_f32_e32 v16, v17, v16
	v_mul_f32_e32 v15, v18, v15
	v_mul_f32_e32 v17, 0x3c800000, v99
	v_mul_f32_e32 v18, 0x3c800000, v136
	v_mul_f32_e32 v19, 0xbfb8aa3b, v18
	v_mul_f32_e32 v15, v17, v15
	v_add_f32_e32 v17, 1.0, v21
	v_exp_f32_e32 v19, v19
	v_rcp_f32_e32 v17, v17
	v_mul_f32_e32 v22, 0x3c800000, v133
	v_mul_f32_e32 v23, 0xbfb8aa3b, v22
	v_add_f32_e32 v19, 1.0, v19
	v_mul_f32_e32 v17, v20, v17
	v_mul_f32_e32 v20, 0x3c800000, v137
	v_rcp_f32_e32 v19, v19
	v_mul_f32_e32 v21, 0xbfb8aa3b, v20
	v_exp_f32_e32 v21, v21
	v_exp_f32_e32 v23, v23
	v_mul_f32_e32 v18, v18, v19
	v_mul_f32_e32 v19, 0x3c800000, v104
	v_mul_f32_e32 v18, v19, v18
	v_mul_f32_e32 v19, 0x3c800000, v100
	v_add_f32_e32 v21, 1.0, v21
	v_rcp_f32_e32 v21, v21
	v_mul_f32_e32 v17, v19, v17
	v_add_f32_e32 v19, 1.0, v23
	v_rcp_f32_e32 v19, v19
	v_mul_f32_e32 v20, v20, v21
	v_mul_f32_e32 v21, 0x3c800000, v105
	v_mul_f32_e32 v20, v21, v20
	v_mul_f32_e32 v19, v22, v19
	v_mul_f32_e32 v21, 0x3c800000, v101
	v_mul_f32_e32 v19, v21, v19
	v_med3_f32 v21, v2, s63, v215
	v_med3_f32 v5, v5, s63, v215
	v_mov_b32_e32 v2, v171
	v_cvt_pk_fp8_f32 v2, v21, v5
	v_med3_f32 v5, v9, s63, v215
	v_med3_f32 v9, v12, s63, v215
	v_med3_f32 v12, v3, s63, v215
	v_med3_f32 v4, v4, s63, v215
	v_mov_b32_e32 v3, v171
	v_cvt_pk_fp8_f32 v3, v12, v4
	v_cvt_pk_fp8_f32 v2, v5, v9 op_sel:[0,0,1]
	v_med3_f32 v4, v8, s63, v215
	v_med3_f32 v5, v11, s63, v215
	v_cvt_pk_fp8_f32 v3, v4, v5 op_sel:[0,0,1]
	v_med3_f32 v5, v14, s63, v215
	v_med3_f32 v8, v16, s63, v215
	v_mov_b32_e32 v4, v171
	v_cvt_pk_fp8_f32 v4, v5, v8
	v_med3_f32 v11, v13, s63, v215
	v_med3_f32 v12, v15, s63, v215
	v_mov_b32_e32 v5, v171
	v_cvt_pk_fp8_f32 v5, v11, v12
	s_add_i32 s21, s21, s50
	v_med3_f32 v8, v18, s63, v215
	v_med3_f32 v9, v20, s63, v215
	s_lshl_b32 s21, s21, 3
	v_cvt_pk_fp8_f32 v4, v8, v9 op_sel:[0,0,1]
	v_med3_f32 v8, v17, s63, v215
	v_med3_f32 v9, v19, s63, v215
	s_add_i32 s28, s21, s49
	v_cvt_pk_fp8_f32 v5, v8, v9 op_sel:[0,0,1]
	s_ashr_i32 s29, s28, 31
	s_lshl_b64 s[28:29], s[28:29], 15
	v_lshl_add_u32 v10, s50, 8, v209
	v_lshl_add_u64 v[6:7], v[178:179], 0, s[28:29]
	v_or_b32_e32 v8, v10, v173
	v_permlane16_swap_b32_e32 v2, v4
	v_permlane16_swap_b32_e32 v3, v5
	v_cmp_gt_i32_e32 vcc, s51, v8
	v_lshl_add_u64 v[8:9], v[6:7], 0, v[180:181]
	s_and_saveexec_b64 s[28:29], vcc
	s_cbranch_execz .LBB0_1066
	global_store_dwordx4 v[8:9], v[2:5], off

; __device__ __forceinline__ unsigned pk4_fp8(float a, float b, float c, float d) { int w = 0; w = __builtin_amdgcn_cvt_pk_fp8_f32(clamp8(a), clamp8(b), w, false); w = __builtin_amdgcn_cvt_pk_fp8_f32(clamp8(c), clamp8(d), w, true); return (unsigned)w; }
;     __device__ __forceinline__ void operator()(AccRef acc, const GUnit& u, int wr, int wc, int fr, int fq) const {
;         const int e = u.x0, rt = u.x1, ct = u.x2, cnt = u.x3; const int* rl = rowlist + (size_t)e * ECAP; const int p0 = rt * 256 + wr * 64 + fr;
;         unsigned ent[2][4];
; #pragma unroll
;         for (int ai = 0; ai < 2; ++ai)
; #pragma unroll
;             for (int m = 0; m < 4; ++m) { int p = p0 + ai * 128 + m * 16; p = p < cnt ? p : cnt - 1; ent[ai][m] = (unsigned)rl[p]; }
; #pragma unroll
;         for (int ai = 0; ai < 2; ++ai)
; #pragma unroll
;             for (int m = 0; m < 4; ++m) { const int p = p0 + ai * 128 + m * 16;
;                 if (p < cnt) { u32x4 w;
; #pragma unroll
;                     for (int q = 0; q < 4; ++q) { const f32x4 v = acc[ai][q >> 1][m][q & 1] * (W8_INV * Y8_SCALE); w[q] = pk4_fp8(v[0], v[1], v[2], v[3]); }
;                     *(u32x4*)(Y + (size_t)ent[ai][m] * D + ct * 256 + wc * 64 + 16 * fq) = w; } }
;     }
.LBB0_1141:
	s_ashr_i32 s23, s22, 31
	s_lshl_b64 s[22:23], s[22:23], 17
	s_add_u32 s26, s49, s22
	v_lshl_add_u32 v16, s66, 8, v186
	s_addc_u32 s27, s50, s23
	s_add_i32 s22, s48, -1
	v_or_b32_e32 v15, 16, v16
	v_min_i32_e32 v2, s22, v15
	v_ashrrev_i32_e32 v3, 31, v2
	v_or_b32_e32 v13, 32, v16
	v_lshl_add_u64 v[18:19], v[2:3], 2, s[26:27]
	v_min_i32_e32 v2, s22, v13
	v_ashrrev_i32_e32 v3, 31, v2
	v_or_b32_e32 v11, 48, v16
	v_lshl_add_u64 v[20:21], v[2:3], 2, s[26:27]
	v_min_i32_e32 v2, s22, v11
	v_ashrrev_i32_e32 v3, 31, v2
	v_add_u32_e32 v9, 0x80, v16
	v_lshl_add_u64 v[22:23], v[2:3], 2, s[26:27]
	v_min_i32_e32 v2, s22, v9
	v_ashrrev_i32_e32 v3, 31, v2
	v_add_u32_e32 v7, 0x90, v16
	v_lshl_add_u64 v[24:25], v[2:3], 2, s[26:27]
	v_min_i32_e32 v2, s22, v7
	v_ashrrev_i32_e32 v3, 31, v2
	v_add_u32_e32 v5, 0xa0, v16
	v_lshl_add_u64 v[26:27], v[2:3], 2, s[26:27]
	v_min_i32_e32 v2, s22, v5
	v_ashrrev_i32_e32 v3, 31, v2
	v_lshl_add_u64 v[28:29], v[2:3], 2, s[26:27]
	v_add_u32_e32 v3, 0xb0, v16
	v_min_i32_e32 v30, s22, v3
	v_ashrrev_i32_e32 v31, 31, v30
	s_nop 15
	s_nop 7
	v_lshl_add_u64 v[30:31], v[30:31], 2, s[26:27]
	global_load_dword v14, v[18:19], off
	global_load_dword v12, v[20:21], off
	global_load_dword v10, v[22:23], off
	global_load_dword v8, v[24:25], off
	global_load_dword v6, v[26:27], off
	global_load_dword v4, v[28:29], off
	global_load_dword v2, v[30:31], off
	s_lshl_b32 s22, s65, 8
	s_ashr_i32 s23, s22, 31
	v_cmp_gt_i32_e32 vcc, s48, v16
	s_and_saveexec_b64 s[24:25], vcc
	s_cbranch_execz .LBB0_1150
	v_ashrrev_i32_e32 v17, 31, v16
	v_lshl_add_u64 v[16:17], v[16:17], 2, s[26:27]
	global_load_dword v176, v[16:17], off
	v_pk_mul_f32 v[16:17], v[158:159], s[14:15] op_sel_hi:[1,0]
	s_nop 0
	v_med3_f32 v18, v16, s59, v193
	v_med3_f32 v17, v17, s59, v193
	v_mov_b32_e32 v16, v177
	v_cvt_pk_fp8_f32 v16, v18, v17
	v_pk_mul_f32 v[18:19], v[160:161], s[14:15] op_sel_hi:[1,0]
	s_nop 0
	v_med3_f32 v17, v18, s59, v193
	v_med3_f32 v18, v19, s59, v193
	v_cvt_pk_fp8_f32 v16, v17, v18 op_sel:[0,0,1]
	v_pk_mul_f32 v[18:19], v[154:155], s[14:15] op_sel_hi:[1,0]
	v_mov_b32_e32 v17, v177
	v_med3_f32 v18, v18, s59, v193
	v_med3_f32 v19, v19, s59, v193
	v_cvt_pk_fp8_f32 v17, v18, v19
	v_pk_mul_f32 v[18:19], v[156:157], s[14:15] op_sel_hi:[1,0]
	s_nop 0
	v_med3_f32 v18, v18, s59, v193
	v_med3_f32 v19, v19, s59, v193
	v_cvt_pk_fp8_f32 v17, v18, v19 op_sel:[0,0,1]
	v_pk_mul_f32 v[18:19], v[150:151], s[14:15] op_sel_hi:[1,0]
	s_nop 0
	v_med3_f32 v20, v18, s59, v193
	v_med3_f32 v19, v19, s59, v193
	v_mov_b32_e32 v18, v177
	v_cvt_pk_fp8_f32 v18, v20, v19
	v_pk_mul_f32 v[20:21], v[152:153], s[14:15] op_sel_hi:[1,0]
	s_nop 0
	v_med3_f32 v19, v20, s59, v193
	v_med3_f32 v20, v21, s59, v193
	v_cvt_pk_fp8_f32 v18, v19, v20 op_sel:[0,0,1]
	v_pk_mul_f32 v[20:21], v[146:147], s[14:15] op_sel_hi:[1,0]
	v_mov_b32_e32 v19, v177
	v_med3_f32 v20, v20, s59, v193
	v_med3_f32 v21, v21, s59, v193
	v_cvt_pk_fp8_f32 v19, v20, v21
	v_pk_mul_f32 v[20:21], v[148:149], s[14:15] op_sel_hi:[1,0]
	s_nop 0
	v_med3_f32 v20, v20, s59, v193
	v_med3_f32 v21, v21, s59, v193
	v_cvt_pk_fp8_f32 v19, v20, v21 op_sel:[0,0,1]
	s_waitcnt vmcnt(0) lgkmcnt(0)
	v_lshlrev_b64 v[20:21], 11, v[176:177]
	v_lshl_add_u64 v[20:21], s[10:11], 0, v[20:21]
	v_lshl_add_u64 v[20:21], v[20:21], 0, s[22:23]
	v_lshl_add_u64 v[20:21], v[20:21], 0, s[6:7]
	v_lshl_add_u64 v[20:21], v[20:21], 0, v[162:163]
	global_store_dwordx4 v[20:21], v[16:19], off
	s_or_b64 exec, exec, s[24:25]
	v_cmp_gt_i32_e32 vcc, s48, v15
	s_and_saveexec_b64 s[24:25], vcc
	s_cbranch_execnz .LBB0_1151
